# plus P0 weight transpose/quantise fast path: batches of 4 w_up/w_down tiles adjacent along k, double-buffered loads, cvt_pk bf16, magic-add int8 rounding (bit-identical results)
# speedup vs baseline: 1.0089x; 1.0064x over previous
; __global__ void __launch_bounds__(NWAVES * 64, 2) fwd(Args args) {
;     ...
;         for (;;) { int base_ = 0; if (lane == 0) base_ = (int)__hip_atomic_fetch_add(CTLP + CW_Q0, 4u, RLX_AGENT); base_ = __builtin_amdgcn_readfirstlane(base_); if (base_ >= NL * I_LAYER) break;
;         for (int it = base_; it < base_ + 4 && it < NL * I_LAYER; ++it) {
;             const int l = it / I_LAYER; int r = it % I_LAYER;
;             const float* Wl = w_in + (size_t)l * D * DIN; bf16* Wt = (bf16*)((unsigned char*)WinT + (size_t)l * NP * D);
;             if (r < I_WIN) {
;                 if (r < I_CKV) { tr_item64<3>(Wl, DIN, SC_CKV, 128, D, Wt, PC_CKV, scr, r, lane); continue; } r -= I_CKV;
;                 if (r < I_QIDX) { tr_item64<3>(Wl, DIN, SC_QIDX, 256, D, Wt, PC_QIDX, scr, r, lane); continue; } r -= I_QIDX;
;                 if (r < I_KIDX) { tr_item64<3>(Wl, DIN, SC_KIDX, 32, D, Wt, PC_KIDX, scr, r, lane); continue; } r -= I_KIDX;
;                 if (r < I_WIDX) { tr_item64<3>(Wl, DIN, SC_WIDX, 8, D, Wt, PC_WIDX, scr, r, lane); continue; } r -= I_WIDX;
;                 if (r < 5 * I_512) { const int s = r / I_512; tr_item64<3>(Wl, DIN, SC_CU + 512 * s, 512, D, Wt, PC_CU + 512 * s, scr, r % I_512, lane); continue; } r -= 5 * I_512;
;                 tr_item64<3>(Wl, DIN, SC_GATE, 4096, D, Wt, PC_GATE, scr, r, lane); continue;
;             }
;             r -= I_WIN;
;             if (r < I_GLU) { tr_item64(IN(18) + (size_t)l * 512 * 512, 512, 0, 512, 512, WgluT + (size_t)l * 512 * 512, 0, scr, r, lane); continue; } r -= I_GLU;
;             if (r < I_MKV) { tr_item64(IN(20) + (size_t)l * 1024 * 1024, 1024, 0, 1024, 1024, WmkvT + (size_t)l * 1024 * 1024, 0, scr, r, lane); continue; } r -= I_MKV;
;             if (r < 4 * I_BR) { const int b = r / I_BR; tr_item64(IN(21) + ((size_t)l * 4 + b) * 512 * 1024, 1024, 0, 1024, 512, WbrT + ((size_t)l * 4 + b) * 1024 * 512, 0, scr, r % I_BR, lane); continue; } r -= 4 * I_BR;
;             if (r < I_WO) { tr_item64(IN(22) + (size_t)l * 1024 * 1024, 1024, 0, 1024, 1024, WoT + (size_t)l * 1024 * 1024, 0, scr, r, lane); continue; } r -= I_WO;
;             if (r < NE * I_UP) { const int e = r / I_UP; tr_item64<1>(IN(27) + ((size_t)l * NE + e) * 1024 * 2048, 2048, 0, 2048, 1024, (bf16*)((unsigned char*)WupT + ((size_t)l * NE + e) * 2048 * 1024), 0, scr, r % I_UP, lane); continue; } r -= NE * I_UP;
.LBB0_69:
	s_or_b64 exec, exec, s[6:7]
	v_readfirstlane_b32 s96, v0
	s_cmp_gt_i32 s96, 0x1acff
	s_mov_b64 s[6:7], -1
	s_cbranch_scc1 .LBB0_64
	s_mov_b32 s41, s97
	s_min_i32 s97, s96, 0x1acfc
	s_add_i32 s97, s97, 4
	s_cmp_ge_i32 s96, s97
	s_cbranch_scc1 .LBB0_63
	s_mul_hi_i32 s6, s96, 0x13187759
	s_lshr_b32 s7, s6, 31
	s_ashr_i32 s6, s6, 11
	s_add_i32 s6, s6, s7
	s_mul_i32 s7, s6, 0xffff94c0
	s_add_i32 s22, s96, s7
	s_cmpk_lt_u32 s22, 0xb40
	s_cbranch_scc1 .Lp0f_slow
	s_lshl_b32 s25, s6, 5
	s_cmpk_lt_u32 s22, 0x4b40
	s_cbranch_scc1 .Lp0f_up
	s_add_i32 s23, s22, 0xffffb4c0
	s_lshr_b32 s24, s23, 8
	s_add_i32 s24, s24, s25
	s_bfe_u32 s25, s23, 0x20006
	s_lshl_b32 s25, s25, 2
	s_bfe_u32 s12, s23, 0x40002
	s_mov_b32 s10, 12
	s_mov_b32 s11, 0x45063f8f
	v_mov_b32_e32 v218, 0x20428
	ds_read_b64 v[218:219], v218
	v_readlane_b32 s8, v255, 11
	v_readlane_b32 s9, v255, 13
	s_lshl_b32 s22, s24, 22
	s_lshl_b32 s23, s24, 20
	s_branch .Lp0f_common
.Lp0f_up:
	s_add_i32 s23, s22, 0xfffff4c0
	s_lshr_b32 s24, s23, 9
	s_add_i32 s24, s24, s25
	s_bfe_u32 s25, s23, 0x20007
	s_lshl_b32 s25, s25, 2
	s_bfe_u32 s12, s23, 0x50002
	s_mov_b32 s10, 13
	s_mov_b32 s11, 0x4461c71c
	v_mov_b32_e32 v218, 0x20418
	ds_read_b64 v[218:219], v218
	v_readlane_b32 s8, v255, 8
	v_readlane_b32 s9, v255, 9
	s_lshl_b32 s22, s24, 23
	s_lshl_b32 s23, s24, 21
.Lp0f_common:
	s_lshl_b32 s24, s25, 6
	s_lshl_b32 s7, s24, s10
	s_add_u32 s22, s22, s7
	s_lshl_b32 s7, s12, 8
	s_add_u32 s22, s22, s7
	s_lshl_b32 s7, s12, 16
	s_add_u32 s23, s23, s7
	s_add_u32 s23, s23, s24
	s_add_u32 s8, s8, s23
	s_addc_u32 s9, s9, 0
	v_mbcnt_lo_u32_b32 v208, -1, 0
	v_mbcnt_hi_u32_b32 v208, -1, v208
	v_lshrrev_b32_e32 v209, 4, v208
	v_and_b32_e32 v210, 15, v208
	v_lshlrev_b32_e32 v211, s10, v209
	v_lshl_add_u32 v211, v210, 4, v211
	v_readlane_b32 s7, v255, 15
	v_mul_u32_u24_e32 v217, 0x88, v209
	v_lshl_add_u32 v212, v210, 3, v217
	v_lshlrev_b32_e32 v214, 10, v210
	v_lshl_add_u32 v214, v209, 3, v214
	s_lshl_b32 s7, s7, 14
	v_add_u32_e32 v212, s7, v212
	v_lshrrev_b32_e32 v217, 2, v210
	v_lshl_add_u32 v217, v209, 3, v217
	v_mul_u32_u24_e32 v217, 0x88, v217
	v_and_b32_e32 v213, 3, v210
	v_lshl_add_u32 v213, v213, 3, v217
	v_add_u32_e32 v213, s7, v213
	v_mov_b32_e32 v215, 0x42fe0000
	v_mov_b32_e32 v216, 0x4b400000
	s_mov_b32 s12, 0xc2fe0000
	s_mov_b32 s24, 0xc0c0400
	s_lshl_b32 s25, 1, s10
	s_lshl_b32 s25, s25, 2
	s_waitcnt lgkmcnt(0)
	v_readfirstlane_b32 s6, v218
	v_readfirstlane_b32 s7, v219
	s_nop 3
	s_add_u32 s22, s6, s22
	s_addc_u32 s23, s7, 0
	s_mov_b64 s[6:7], s[22:23]
	global_load_dwordx4 v[144:147], v211, s[6:7] offset:0 nt
	s_add_u32 s6, s6, s25
	s_addc_u32 s7, s7, 0
	global_load_dwordx4 v[148:151], v211, s[6:7] offset:0 nt
	s_add_u32 s6, s6, s25
	s_addc_u32 s7, s7, 0
	global_load_dwordx4 v[152:155], v211, s[6:7] offset:0 nt
	s_add_u32 s6, s6, s25
	s_addc_u32 s7, s7, 0
	global_load_dwordx4 v[156:159], v211, s[6:7] offset:0 nt
	s_add_u32 s6, s6, s25
	s_addc_u32 s7, s7, 0
	global_load_dwordx4 v[160:163], v211, s[6:7] offset:0 nt
	s_add_u32 s6, s6, s25
	s_addc_u32 s7, s7, 0
	global_load_dwordx4 v[164:167], v211, s[6:7] offset:0 nt
	s_add_u32 s6, s6, s25
	s_addc_u32 s7, s7, 0
	global_load_dwordx4 v[168:171], v211, s[6:7] offset:0 nt
	s_add_u32 s6, s6, s25
	s_addc_u32 s7, s7, 0
	global_load_dwordx4 v[172:175], v211, s[6:7] offset:0 nt
	s_add_u32 s6, s6, s25
	s_addc_u32 s7, s7, 0
	global_load_dwordx4 v[176:179], v211, s[6:7] offset:0 nt
	s_add_u32 s6, s6, s25
	s_addc_u32 s7, s7, 0
	global_load_dwordx4 v[180:183], v211, s[6:7] offset:0 nt
	s_add_u32 s6, s6, s25
	s_addc_u32 s7, s7, 0
	global_load_dwordx4 v[184:187], v211, s[6:7] offset:0 nt
	s_add_u32 s6, s6, s25
	s_addc_u32 s7, s7, 0
	global_load_dwordx4 v[188:191], v211, s[6:7] offset:0 nt
	s_add_u32 s6, s6, s25
	s_addc_u32 s7, s7, 0
	global_load_dwordx4 v[192:195], v211, s[6:7] offset:0 nt
	s_add_u32 s6, s6, s25
	s_addc_u32 s7, s7, 0
	global_load_dwordx4 v[196:199], v211, s[6:7] offset:0 nt
	s_add_u32 s6, s6, s25
	s_addc_u32 s7, s7, 0
	global_load_dwordx4 v[200:203], v211, s[6:7] offset:0 nt
	s_add_u32 s6, s6, s25
	s_addc_u32 s7, s7, 0
	global_load_dwordx4 v[204:207], v211, s[6:7] offset:0 nt
	s_mul_i32 s26, s25, 16
	s_add_u32 s6, s22, s26
	s_addc_u32 s7, s23, 0
	global_load_dwordx4 v[0:3], v211, s[6:7] offset:0 nt
	s_add_u32 s6, s6, s25
	s_addc_u32 s7, s7, 0
	global_load_dwordx4 v[4:7], v211, s[6:7] offset:0 nt
	s_add_u32 s6, s6, s25
	s_addc_u32 s7, s7, 0
	global_load_dwordx4 v[8:11], v211, s[6:7] offset:0 nt
	s_add_u32 s6, s6, s25
	s_addc_u32 s7, s7, 0
	global_load_dwordx4 v[12:15], v211, s[6:7] offset:0 nt
	s_add_u32 s6, s6, s25
	s_addc_u32 s7, s7, 0
	global_load_dwordx4 v[16:19], v211, s[6:7] offset:0 nt
	s_add_u32 s6, s6, s25
	s_addc_u32 s7, s7, 0
	global_load_dwordx4 v[20:23], v211, s[6:7] offset:0 nt
	s_add_u32 s6, s6, s25
	s_addc_u32 s7, s7, 0
	global_load_dwordx4 v[24:27], v211, s[6:7] offset:0 nt
	s_add_u32 s6, s6, s25
	s_addc_u32 s7, s7, 0
	global_load_dwordx4 v[28:31], v211, s[6:7] offset:0 nt
	s_add_u32 s6, s6, s25
	s_addc_u32 s7, s7, 0
	global_load_dwordx4 v[32:35], v211, s[6:7] offset:0 nt
	s_add_u32 s6, s6, s25
	s_addc_u32 s7, s7, 0
	global_load_dwordx4 v[36:39], v211, s[6:7] offset:0 nt
	s_add_u32 s6, s6, s25
	s_addc_u32 s7, s7, 0
	global_load_dwordx4 v[40:43], v211, s[6:7] offset:0 nt
	s_add_u32 s6, s6, s25
	s_addc_u32 s7, s7, 0
	global_load_dwordx4 v[44:47], v211, s[6:7] offset:0 nt
	s_add_u32 s6, s6, s25
	s_addc_u32 s7, s7, 0
	global_load_dwordx4 v[48:51], v211, s[6:7] offset:0 nt
	s_add_u32 s6, s6, s25
	s_addc_u32 s7, s7, 0
	global_load_dwordx4 v[52:55], v211, s[6:7] offset:0 nt
	s_add_u32 s6, s6, s25
	s_addc_u32 s7, s7, 0
	global_load_dwordx4 v[56:59], v211, s[6:7] offset:0 nt
	s_add_u32 s6, s6, s25
	s_addc_u32 s7, s7, 0
	global_load_dwordx4 v[60:63], v211, s[6:7] offset:0 nt
	s_mul_i32 s26, s25, 32
	s_add_u32 s6, s22, s26
	s_addc_u32 s7, s23, 0
	s_waitcnt vmcnt(31)
; #define LAS __attribute__((address_space(3)))
; #define LDS_WAIT() asm volatile("s_waitcnt lgkmcnt(0)" ::: "memory")
; __device__ __forceinline__ unsigned pk2(float lo, float hi) { return f2bf(lo) | (f2bf(hi) << 16); }
; __device__ __forceinline__ unsigned q8x4(float a, float b, float c, float d, float s) { return q8_(a, s) | (q8_(b, s) << 8) | (q8_(c, s) << 16) | (q8_(d, s) << 24); }
;     ...
;     for (int i = 0; i < 16; ++i) { vv[i] = (f32x4){0.f, 0.f, 0.f, 0.f}; if (okn) vv[i] = __builtin_nontemporal_load((const f32x4*)(wp + (size_t)(4 * i) * ldw)); }
; #pragma unroll
;     for (int i = 0; i < 16; ++i) { v2u w2; w2.x = pk2(vv[i][0], vv[i][1]); w2.y = pk2(vv[i][2], vv[i][3]); *(LAS v2u*)(scr + (4 * i + g) * 136 + nn * 2) = w2; }
;     LDS_WAIT(); asm volatile("" ::: "memory");
;     const int i16 = lane & 15, q = i16 >> 2, p = i16 & 3;
; #pragma unroll
;     for (int s = 0; s < 8; ++s) { const int nbk = s & 3, kbk = 4 * (s >> 2) + g;
;         const v4i16_t lo = __builtin_amdgcn_ds_read_tr16_b64_v4i16((LAS v4i16_t*)(scr + (8 * kbk + q) * 136 + 32 * nbk + 8 * p));
;         const v4i16_t hi = __builtin_amdgcn_ds_read_tr16_b64_v4i16((LAS v4i16_t*)(scr + (8 * kbk + 4 + q) * 136 + 32 * nbk + 8 * p));
;         const bf16x8 o = __builtin_shufflevector(lo, hi, 0, 1, 2, 3, 4, 5, 6, 7); const int n = 16 * nbk + i16;
;         if (n0 + n < nc) {
;             if constexpr (QMODE == 0) *(bf16x8*)(WT + (size_t)(r0 + n0 + n) * K + k0 + 8 * kbk) = o;
;             else { const v4u ou = __builtin_bit_cast(v4u, o); const float sc_ = QMODE == 1 ? QS_WUP : (QMODE == 2 ? QS_WDN : QS_WIN);
;                 *(v2u*)((unsigned char*)WT + (size_t)(r0 + n0 + n) * K + k0 + 8 * kbk) = (v2u){q8x4(bflo(ou.x), bfhi(ou.x), bflo(ou.y), bfhi(ou.y), sc_), q8x4(bflo(ou.z), bfhi(ou.z), bflo(ou.w), bfhi(ou.w), sc_)}; } } }
	v_cvt_pk_bf16_f32 v220, v144, v145
	v_cvt_pk_bf16_f32 v221, v146, v147
	ds_write_b64 v212, v[220:221] offset:0
	global_load_dwordx4 v[144:147], v211, s[6:7] offset:0 nt
	s_add_u32 s6, s6, s25
	s_addc_u32 s7, s7, 0
	s_waitcnt vmcnt(31)
	v_cvt_pk_bf16_f32 v220, v148, v149
	v_cvt_pk_bf16_f32 v221, v150, v151
	ds_write_b64 v212, v[220:221] offset:544
	global_load_dwordx4 v[148:151], v211, s[6:7] offset:0 nt
	s_add_u32 s6, s6, s25
	s_addc_u32 s7, s7, 0
	s_waitcnt vmcnt(31)
	v_cvt_pk_bf16_f32 v220, v152, v153
	v_cvt_pk_bf16_f32 v221, v154, v155
	ds_write_b64 v212, v[220:221] offset:1088
	global_load_dwordx4 v[152:155], v211, s[6:7] offset:0 nt
	s_add_u32 s6, s6, s25
	s_addc_u32 s7, s7, 0
	s_waitcnt vmcnt(31)
	v_cvt_pk_bf16_f32 v220, v156, v157
	v_cvt_pk_bf16_f32 v221, v158, v159
	ds_write_b64 v212, v[220:221] offset:1632
	global_load_dwordx4 v[156:159], v211, s[6:7] offset:0 nt
	s_add_u32 s6, s6, s25
	s_addc_u32 s7, s7, 0
	s_waitcnt vmcnt(31)
	v_cvt_pk_bf16_f32 v220, v160, v161
	v_cvt_pk_bf16_f32 v221, v162, v163
	ds_write_b64 v212, v[220:221] offset:2176
	global_load_dwordx4 v[160:163], v211, s[6:7] offset:0 nt
	s_add_u32 s6, s6, s25
	s_addc_u32 s7, s7, 0
	s_waitcnt vmcnt(31)
	v_cvt_pk_bf16_f32 v220, v164, v165
	v_cvt_pk_bf16_f32 v221, v166, v167
	ds_write_b64 v212, v[220:221] offset:2720
	global_load_dwordx4 v[164:167], v211, s[6:7] offset:0 nt
	s_add_u32 s6, s6, s25
	s_addc_u32 s7, s7, 0
	s_waitcnt vmcnt(31)
	v_cvt_pk_bf16_f32 v220, v168, v169
	v_cvt_pk_bf16_f32 v221, v170, v171
	ds_write_b64 v212, v[220:221] offset:3264
	global_load_dwordx4 v[168:171], v211, s[6:7] offset:0 nt
	s_add_u32 s6, s6, s25
	s_addc_u32 s7, s7, 0
	s_waitcnt vmcnt(31)
	v_cvt_pk_bf16_f32 v220, v172, v173
	v_cvt_pk_bf16_f32 v221, v174, v175
	ds_write_b64 v212, v[220:221] offset:3808
	global_load_dwordx4 v[172:175], v211, s[6:7] offset:0 nt
	s_add_u32 s6, s6, s25
	s_addc_u32 s7, s7, 0
	s_waitcnt vmcnt(31)
	v_cvt_pk_bf16_f32 v220, v176, v177
	v_cvt_pk_bf16_f32 v221, v178, v179
	ds_write_b64 v212, v[220:221] offset:4352
	global_load_dwordx4 v[176:179], v211, s[6:7] offset:0 nt
	s_add_u32 s6, s6, s25
	s_addc_u32 s7, s7, 0
	s_waitcnt vmcnt(31)
	v_cvt_pk_bf16_f32 v220, v180, v181
	v_cvt_pk_bf16_f32 v221, v182, v183
	ds_write_b64 v212, v[220:221] offset:4896
	global_load_dwordx4 v[180:183], v211, s[6:7] offset:0 nt
	s_add_u32 s6, s6, s25
	s_addc_u32 s7, s7, 0
	s_waitcnt vmcnt(31)
	v_cvt_pk_bf16_f32 v220, v184, v185
	v_cvt_pk_bf16_f32 v221, v186, v187
	ds_write_b64 v212, v[220:221] offset:5440
	s_waitcnt lgkmcnt(8)
	global_load_dwordx4 v[184:187], v211, s[6:7] offset:0 nt
	s_add_u32 s6, s6, s25
	s_addc_u32 s7, s7, 0
	s_waitcnt vmcnt(31)
	v_cvt_pk_bf16_f32 v220, v188, v189
	v_cvt_pk_bf16_f32 v221, v190, v191
	ds_write_b64 v212, v[220:221] offset:5984
	s_waitcnt lgkmcnt(8)
	global_load_dwordx4 v[188:191], v211, s[6:7] offset:0 nt
	s_add_u32 s6, s6, s25
	s_addc_u32 s7, s7, 0
	s_waitcnt vmcnt(31)
	v_cvt_pk_bf16_f32 v220, v192, v193
	v_cvt_pk_bf16_f32 v221, v194, v195
	ds_write_b64 v212, v[220:221] offset:6528
	s_waitcnt lgkmcnt(8)
	global_load_dwordx4 v[192:195], v211, s[6:7] offset:0 nt
	s_add_u32 s6, s6, s25
	s_addc_u32 s7, s7, 0
	s_waitcnt vmcnt(31)
	v_cvt_pk_bf16_f32 v220, v196, v197
	v_cvt_pk_bf16_f32 v221, v198, v199
	ds_write_b64 v212, v[220:221] offset:7072
	s_waitcnt lgkmcnt(8)
	global_load_dwordx4 v[196:199], v211, s[6:7] offset:0 nt
	s_add_u32 s6, s6, s25
	s_addc_u32 s7, s7, 0
	s_waitcnt vmcnt(31)
	v_cvt_pk_bf16_f32 v220, v200, v201
	v_cvt_pk_bf16_f32 v221, v202, v203
	ds_write_b64 v212, v[220:221] offset:7616
	s_waitcnt lgkmcnt(8)
	global_load_dwordx4 v[200:203], v211, s[6:7] offset:0 nt
	s_add_u32 s6, s6, s25
	s_addc_u32 s7, s7, 0
	s_waitcnt vmcnt(31)
	v_cvt_pk_bf16_f32 v220, v204, v205
	v_cvt_pk_bf16_f32 v221, v206, v207
	ds_write_b64 v212, v[220:221] offset:8160
	global_load_dwordx4 v[204:207], v211, s[6:7] offset:0 nt
	s_waitcnt lgkmcnt(0)
	ds_read_b64_tr_b16 v[222:223], v213 offset:0
	ds_read_b64_tr_b16 v[224:225], v213 offset:544
	ds_read_b64_tr_b16 v[226:227], v213 offset:4352
	ds_read_b64_tr_b16 v[228:229], v213 offset:4896
	ds_read_b64_tr_b16 v[230:231], v213 offset:32
	ds_read_b64_tr_b16 v[232:233], v213 offset:576
	ds_read_b64_tr_b16 v[234:235], v213 offset:4384
	ds_read_b64_tr_b16 v[236:237], v213 offset:4928
	s_waitcnt lgkmcnt(6)
	v_lshlrev_b32_e32 v238, 16, v222
	v_and_b32_e32 v239, 0xffff0000, v222
	v_lshlrev_b32_e32 v240, 16, v223
	v_and_b32_e32 v241, 0xffff0000, v223
	v_mul_f32_e32 v238, s11, v238
	v_mul_f32_e32 v239, s11, v239
	v_mul_f32_e32 v240, s11, v240
	v_mul_f32_e32 v241, s11, v241
	v_med3_f32 v238, v238, s12, v215
	v_med3_f32 v239, v239, s12, v215
	v_med3_f32 v240, v240, s12, v215
	v_med3_f32 v241, v241, s12, v215
	v_add_f32_e32 v238, v216, v238
	v_add_f32_e32 v239, v216, v239
	v_add_f32_e32 v240, v216, v240
	v_add_f32_e32 v241, v216, v241
	v_perm_b32 v238, v239, v238, s24
	v_perm_b32 v240, v241, v240, s24
	v_lshl_or_b32 v246, v240, 16, v238
	v_lshlrev_b32_e32 v238, 16, v224
	v_and_b32_e32 v239, 0xffff0000, v224
	v_lshlrev_b32_e32 v240, 16, v225
	v_and_b32_e32 v241, 0xffff0000, v225
	v_mul_f32_e32 v238, s11, v238
	v_mul_f32_e32 v239, s11, v239
	v_mul_f32_e32 v240, s11, v240
	v_mul_f32_e32 v241, s11, v241
	v_med3_f32 v238, v238, s12, v215
	v_med3_f32 v239, v239, s12, v215
	v_med3_f32 v240, v240, s12, v215
	v_med3_f32 v241, v241, s12, v215
	v_add_f32_e32 v238, v216, v238
	v_add_f32_e32 v239, v216, v239
	v_add_f32_e32 v240, v216, v240
	v_add_f32_e32 v241, v216, v241
	v_perm_b32 v238, v239, v238, s24
	v_perm_b32 v240, v241, v240, s24
	v_lshl_or_b32 v247, v240, 16, v238
	global_store_dwordx2 v214, v[246:247], s[8:9]
	s_waitcnt lgkmcnt(4)
; #define LAS __attribute__((address_space(3)))
; __device__ __forceinline__ unsigned q8x4(float a, float b, float c, float d, float s) { return q8_(a, s) | (q8_(b, s) << 8) | (q8_(c, s) << 16) | (q8_(d, s) << 24); }
;     ...
;     const int i16 = lane & 15, q = i16 >> 2, p = i16 & 3;
; #pragma unroll
;     for (int s = 0; s < 8; ++s) { const int nbk = s & 3, kbk = 4 * (s >> 2) + g;
;         const v4i16_t lo = __builtin_amdgcn_ds_read_tr16_b64_v4i16((LAS v4i16_t*)(scr + (8 * kbk + q) * 136 + 32 * nbk + 8 * p));
;         const v4i16_t hi = __builtin_amdgcn_ds_read_tr16_b64_v4i16((LAS v4i16_t*)(scr + (8 * kbk + 4 + q) * 136 + 32 * nbk + 8 * p));
;         const bf16x8 o = __builtin_shufflevector(lo, hi, 0, 1, 2, 3, 4, 5, 6, 7); const int n = 16 * nbk + i16;
;         if (n0 + n < nc) {
;             if constexpr (QMODE == 0) *(bf16x8*)(WT + (size_t)(r0 + n0 + n) * K + k0 + 8 * kbk) = o;
;             else { const v4u ou = __builtin_bit_cast(v4u, o); const float sc_ = QMODE == 1 ? QS_WUP : (QMODE == 2 ? QS_WDN : QS_WIN);
;                 *(v2u*)((unsigned char*)WT + (size_t)(r0 + n0 + n) * K + k0 + 8 * kbk) = (v2u){q8x4(bflo(ou.x), bfhi(ou.x), bflo(ou.y), bfhi(ou.y), sc_), q8x4(bflo(ou.z), bfhi(ou.z), bflo(ou.w), bfhi(ou.w), sc_)}; } } }
	v_lshlrev_b32_e32 v238, 16, v226
	v_and_b32_e32 v239, 0xffff0000, v226
	v_lshlrev_b32_e32 v240, 16, v227
	v_and_b32_e32 v241, 0xffff0000, v227
	v_mul_f32_e32 v238, s11, v238
	v_mul_f32_e32 v239, s11, v239
	v_mul_f32_e32 v240, s11, v240
	v_mul_f32_e32 v241, s11, v241
	v_med3_f32 v238, v238, s12, v215
	v_med3_f32 v239, v239, s12, v215
	v_med3_f32 v240, v240, s12, v215
	v_med3_f32 v241, v241, s12, v215
	v_add_f32_e32 v238, v216, v238
	v_add_f32_e32 v239, v216, v239
	v_add_f32_e32 v240, v216, v240
	v_add_f32_e32 v241, v216, v241
	v_perm_b32 v238, v239, v238, s24
	v_perm_b32 v240, v241, v240, s24
	v_lshl_or_b32 v248, v240, 16, v238
	v_lshlrev_b32_e32 v238, 16, v228
	v_and_b32_e32 v239, 0xffff0000, v228
	v_lshlrev_b32_e32 v240, 16, v229
	v_and_b32_e32 v241, 0xffff0000, v229
	v_mul_f32_e32 v238, s11, v238
	v_mul_f32_e32 v239, s11, v239
	v_mul_f32_e32 v240, s11, v240
	v_mul_f32_e32 v241, s11, v241
	v_med3_f32 v238, v238, s12, v215
	v_med3_f32 v239, v239, s12, v215
	v_med3_f32 v240, v240, s12, v215
	v_med3_f32 v241, v241, s12, v215
	v_add_f32_e32 v238, v216, v238
	v_add_f32_e32 v239, v216, v239
	v_add_f32_e32 v240, v216, v240
	v_add_f32_e32 v241, v216, v241
	v_perm_b32 v238, v239, v238, s24
	v_perm_b32 v240, v241, v240, s24
	v_lshl_or_b32 v249, v240, 16, v238
	global_store_dwordx2 v214, v[248:249], s[8:9] offset:32
	ds_read_b64_tr_b16 v[222:223], v213 offset:64
	ds_read_b64_tr_b16 v[224:225], v213 offset:608
	ds_read_b64_tr_b16 v[226:227], v213 offset:4416
	ds_read_b64_tr_b16 v[228:229], v213 offset:4960
	s_add_u32 s8, s8, 0x4000
	s_addc_u32 s9, s9, 0
	s_waitcnt lgkmcnt(6)
	v_lshlrev_b32_e32 v238, 16, v230
	v_and_b32_e32 v239, 0xffff0000, v230
	v_lshlrev_b32_e32 v240, 16, v231
	v_and_b32_e32 v241, 0xffff0000, v231
	v_mul_f32_e32 v238, s11, v238
	v_mul_f32_e32 v239, s11, v239
	v_mul_f32_e32 v240, s11, v240
	v_mul_f32_e32 v241, s11, v241
	v_med3_f32 v238, v238, s12, v215
	v_med3_f32 v239, v239, s12, v215
	v_med3_f32 v240, v240, s12, v215
	v_med3_f32 v241, v241, s12, v215
	v_add_f32_e32 v238, v216, v238
	v_add_f32_e32 v239, v216, v239
	v_add_f32_e32 v240, v216, v240
	v_add_f32_e32 v241, v216, v241
	v_perm_b32 v238, v239, v238, s24
	v_perm_b32 v240, v241, v240, s24
	v_lshl_or_b32 v246, v240, 16, v238
	v_lshlrev_b32_e32 v238, 16, v232
	v_and_b32_e32 v239, 0xffff0000, v232
	v_lshlrev_b32_e32 v240, 16, v233
	v_and_b32_e32 v241, 0xffff0000, v233
	v_mul_f32_e32 v238, s11, v238
	v_mul_f32_e32 v239, s11, v239
	v_mul_f32_e32 v240, s11, v240
	v_mul_f32_e32 v241, s11, v241
	v_med3_f32 v238, v238, s12, v215
	v_med3_f32 v239, v239, s12, v215
	v_med3_f32 v240, v240, s12, v215
	v_med3_f32 v241, v241, s12, v215
	v_add_f32_e32 v238, v216, v238
	v_add_f32_e32 v239, v216, v239
	v_add_f32_e32 v240, v216, v240
	v_add_f32_e32 v241, v216, v241
	v_perm_b32 v238, v239, v238, s24
	v_perm_b32 v240, v241, v240, s24
	v_lshl_or_b32 v247, v240, 16, v238
	global_store_dwordx2 v214, v[246:247], s[8:9]
	s_waitcnt lgkmcnt(4)
	v_lshlrev_b32_e32 v238, 16, v234
	v_and_b32_e32 v239, 0xffff0000, v234
	v_lshlrev_b32_e32 v240, 16, v235
	v_and_b32_e32 v241, 0xffff0000, v235
	v_mul_f32_e32 v238, s11, v238
	v_mul_f32_e32 v239, s11, v239
	v_mul_f32_e32 v240, s11, v240
	v_mul_f32_e32 v241, s11, v241
	v_med3_f32 v238, v238, s12, v215
	v_med3_f32 v239, v239, s12, v215
	v_med3_f32 v240, v240, s12, v215
	v_med3_f32 v241, v241, s12, v215
	v_add_f32_e32 v238, v216, v238
	v_add_f32_e32 v239, v216, v239
	v_add_f32_e32 v240, v216, v240
	v_add_f32_e32 v241, v216, v241
	v_perm_b32 v238, v239, v238, s24
	v_perm_b32 v240, v241, v240, s24
	v_lshl_or_b32 v248, v240, 16, v238
	v_lshlrev_b32_e32 v238, 16, v236
	v_and_b32_e32 v239, 0xffff0000, v236
	v_lshlrev_b32_e32 v240, 16, v237
	v_and_b32_e32 v241, 0xffff0000, v237
	v_mul_f32_e32 v238, s11, v238
	v_mul_f32_e32 v239, s11, v239
	v_mul_f32_e32 v240, s11, v240
	v_mul_f32_e32 v241, s11, v241
	v_med3_f32 v238, v238, s12, v215
	v_med3_f32 v239, v239, s12, v215
	v_med3_f32 v240, v240, s12, v215
	v_med3_f32 v241, v241, s12, v215
	v_add_f32_e32 v238, v216, v238
	v_add_f32_e32 v239, v216, v239
	v_add_f32_e32 v240, v216, v240
	v_add_f32_e32 v241, v216, v241
	v_perm_b32 v238, v239, v238, s24
	v_perm_b32 v240, v241, v240, s24
	v_lshl_or_b32 v249, v240, 16, v238
	global_store_dwordx2 v214, v[248:249], s[8:9] offset:32
	ds_read_b64_tr_b16 v[230:231], v213 offset:96
	ds_read_b64_tr_b16 v[232:233], v213 offset:640
	ds_read_b64_tr_b16 v[234:235], v213 offset:4448
	ds_read_b64_tr_b16 v[236:237], v213 offset:4992
	s_add_u32 s8, s8, 0x4000
	s_addc_u32 s9, s9, 0
	s_waitcnt lgkmcnt(6)
	v_lshlrev_b32_e32 v238, 16, v222
	v_and_b32_e32 v239, 0xffff0000, v222
	v_lshlrev_b32_e32 v240, 16, v223
	v_and_b32_e32 v241, 0xffff0000, v223
	v_mul_f32_e32 v238, s11, v238
	v_mul_f32_e32 v239, s11, v239
	v_mul_f32_e32 v240, s11, v240
	v_mul_f32_e32 v241, s11, v241
	v_med3_f32 v238, v238, s12, v215
	v_med3_f32 v239, v239, s12, v215
	v_med3_f32 v240, v240, s12, v215
	v_med3_f32 v241, v241, s12, v215
	v_add_f32_e32 v238, v216, v238
	v_add_f32_e32 v239, v216, v239
	v_add_f32_e32 v240, v216, v240
	v_add_f32_e32 v241, v216, v241
	v_perm_b32 v238, v239, v238, s24
	v_perm_b32 v240, v241, v240, s24
	v_lshl_or_b32 v246, v240, 16, v238
	v_lshlrev_b32_e32 v238, 16, v224
	v_and_b32_e32 v239, 0xffff0000, v224
	v_lshlrev_b32_e32 v240, 16, v225
	v_and_b32_e32 v241, 0xffff0000, v225
	v_mul_f32_e32 v238, s11, v238
	v_mul_f32_e32 v239, s11, v239
	v_mul_f32_e32 v240, s11, v240
	v_mul_f32_e32 v241, s11, v241
	v_med3_f32 v238, v238, s12, v215
	v_med3_f32 v239, v239, s12, v215
	v_med3_f32 v240, v240, s12, v215
	v_med3_f32 v241, v241, s12, v215
	v_add_f32_e32 v238, v216, v238
	v_add_f32_e32 v239, v216, v239
	v_add_f32_e32 v240, v216, v240
	v_add_f32_e32 v241, v216, v241
	v_perm_b32 v238, v239, v238, s24
	v_perm_b32 v240, v241, v240, s24
	v_lshl_or_b32 v247, v240, 16, v238
	global_store_dwordx2 v214, v[246:247], s[8:9]
	s_waitcnt lgkmcnt(4)
; #define LAS __attribute__((address_space(3)))
; __device__ __forceinline__ unsigned pk2(float lo, float hi) { return f2bf(lo) | (f2bf(hi) << 16); }
; __device__ __forceinline__ unsigned q8x4(float a, float b, float c, float d, float s) { return q8_(a, s) | (q8_(b, s) << 8) | (q8_(c, s) << 16) | (q8_(d, s) << 24); }
;     ...
;     for (int i = 0; i < 16; ++i) { vv[i] = (f32x4){0.f, 0.f, 0.f, 0.f}; if (okn) vv[i] = __builtin_nontemporal_load((const f32x4*)(wp + (size_t)(4 * i) * ldw)); }
; #pragma unroll
;     for (int i = 0; i < 16; ++i) { v2u w2; w2.x = pk2(vv[i][0], vv[i][1]); w2.y = pk2(vv[i][2], vv[i][3]); *(LAS v2u*)(scr + (4 * i + g) * 136 + nn * 2) = w2; }
;     ...
;     const int i16 = lane & 15, q = i16 >> 2, p = i16 & 3;
; #pragma unroll
;     for (int s = 0; s < 8; ++s) { const int nbk = s & 3, kbk = 4 * (s >> 2) + g;
;         const v4i16_t lo = __builtin_amdgcn_ds_read_tr16_b64_v4i16((LAS v4i16_t*)(scr + (8 * kbk + q) * 136 + 32 * nbk + 8 * p));
;         const v4i16_t hi = __builtin_amdgcn_ds_read_tr16_b64_v4i16((LAS v4i16_t*)(scr + (8 * kbk + 4 + q) * 136 + 32 * nbk + 8 * p));
;         const bf16x8 o = __builtin_shufflevector(lo, hi, 0, 1, 2, 3, 4, 5, 6, 7); const int n = 16 * nbk + i16;
;         if (n0 + n < nc) {
;             if constexpr (QMODE == 0) *(bf16x8*)(WT + (size_t)(r0 + n0 + n) * K + k0 + 8 * kbk) = o;
;             else { const v4u ou = __builtin_bit_cast(v4u, o); const float sc_ = QMODE == 1 ? QS_WUP : (QMODE == 2 ? QS_WDN : QS_WIN);
;                 *(v2u*)((unsigned char*)WT + (size_t)(r0 + n0 + n) * K + k0 + 8 * kbk) = (v2u){q8x4(bflo(ou.x), bfhi(ou.x), bflo(ou.y), bfhi(ou.y), sc_), q8x4(bflo(ou.z), bfhi(ou.z), bflo(ou.w), bfhi(ou.w), sc_)}; } } }
	v_lshlrev_b32_e32 v238, 16, v226
	v_and_b32_e32 v239, 0xffff0000, v226
	v_lshlrev_b32_e32 v240, 16, v227
	v_and_b32_e32 v241, 0xffff0000, v227
	v_mul_f32_e32 v238, s11, v238
	v_mul_f32_e32 v239, s11, v239
	v_mul_f32_e32 v240, s11, v240
	v_mul_f32_e32 v241, s11, v241
	v_med3_f32 v238, v238, s12, v215
	v_med3_f32 v239, v239, s12, v215
	v_med3_f32 v240, v240, s12, v215
	v_med3_f32 v241, v241, s12, v215
	v_add_f32_e32 v238, v216, v238
	v_add_f32_e32 v239, v216, v239
	v_add_f32_e32 v240, v216, v240
	v_add_f32_e32 v241, v216, v241
	v_perm_b32 v238, v239, v238, s24
	v_perm_b32 v240, v241, v240, s24
	v_lshl_or_b32 v248, v240, 16, v238
	v_lshlrev_b32_e32 v238, 16, v228
	v_and_b32_e32 v239, 0xffff0000, v228
	v_lshlrev_b32_e32 v240, 16, v229
	v_and_b32_e32 v241, 0xffff0000, v229
	v_mul_f32_e32 v238, s11, v238
	v_mul_f32_e32 v239, s11, v239
	v_mul_f32_e32 v240, s11, v240
	v_mul_f32_e32 v241, s11, v241
	v_med3_f32 v238, v238, s12, v215
	v_med3_f32 v239, v239, s12, v215
	v_med3_f32 v240, v240, s12, v215
	v_med3_f32 v241, v241, s12, v215
	v_add_f32_e32 v238, v216, v238
	v_add_f32_e32 v239, v216, v239
	v_add_f32_e32 v240, v216, v240
	v_add_f32_e32 v241, v216, v241
	v_perm_b32 v238, v239, v238, s24
	v_perm_b32 v240, v241, v240, s24
	v_lshl_or_b32 v249, v240, 16, v238
	global_store_dwordx2 v214, v[248:249], s[8:9] offset:32
	s_add_u32 s8, s8, 0x4000
	s_addc_u32 s9, s9, 0
	s_waitcnt lgkmcnt(2)
	v_lshlrev_b32_e32 v238, 16, v230
	v_and_b32_e32 v239, 0xffff0000, v230
	v_lshlrev_b32_e32 v240, 16, v231
	v_and_b32_e32 v241, 0xffff0000, v231
	v_mul_f32_e32 v238, s11, v238
	v_mul_f32_e32 v239, s11, v239
	v_mul_f32_e32 v240, s11, v240
	v_mul_f32_e32 v241, s11, v241
	v_med3_f32 v238, v238, s12, v215
	v_med3_f32 v239, v239, s12, v215
	v_med3_f32 v240, v240, s12, v215
	v_med3_f32 v241, v241, s12, v215
	v_add_f32_e32 v238, v216, v238
	v_add_f32_e32 v239, v216, v239
	v_add_f32_e32 v240, v216, v240
	v_add_f32_e32 v241, v216, v241
	v_perm_b32 v238, v239, v238, s24
	v_perm_b32 v240, v241, v240, s24
	v_lshl_or_b32 v246, v240, 16, v238
	v_lshlrev_b32_e32 v238, 16, v232
	v_and_b32_e32 v239, 0xffff0000, v232
	v_lshlrev_b32_e32 v240, 16, v233
	v_and_b32_e32 v241, 0xffff0000, v233
	v_mul_f32_e32 v238, s11, v238
	v_mul_f32_e32 v239, s11, v239
	v_mul_f32_e32 v240, s11, v240
	v_mul_f32_e32 v241, s11, v241
	v_med3_f32 v238, v238, s12, v215
	v_med3_f32 v239, v239, s12, v215
	v_med3_f32 v240, v240, s12, v215
	v_med3_f32 v241, v241, s12, v215
	v_add_f32_e32 v238, v216, v238
	v_add_f32_e32 v239, v216, v239
	v_add_f32_e32 v240, v216, v240
	v_add_f32_e32 v241, v216, v241
	v_perm_b32 v238, v239, v238, s24
	v_perm_b32 v240, v241, v240, s24
	v_lshl_or_b32 v247, v240, 16, v238
	global_store_dwordx2 v214, v[246:247], s[8:9]
	s_waitcnt lgkmcnt(0)
	v_lshlrev_b32_e32 v238, 16, v234
	v_and_b32_e32 v239, 0xffff0000, v234
	v_lshlrev_b32_e32 v240, 16, v235
	v_and_b32_e32 v241, 0xffff0000, v235
	v_mul_f32_e32 v238, s11, v238
	v_mul_f32_e32 v239, s11, v239
	v_mul_f32_e32 v240, s11, v240
	v_mul_f32_e32 v241, s11, v241
	v_med3_f32 v238, v238, s12, v215
	v_med3_f32 v239, v239, s12, v215
	v_med3_f32 v240, v240, s12, v215
	v_med3_f32 v241, v241, s12, v215
	v_add_f32_e32 v238, v216, v238
	v_add_f32_e32 v239, v216, v239
	v_add_f32_e32 v240, v216, v240
	v_add_f32_e32 v241, v216, v241
	v_perm_b32 v238, v239, v238, s24
	v_perm_b32 v240, v241, v240, s24
	v_lshl_or_b32 v248, v240, 16, v238
	v_lshlrev_b32_e32 v238, 16, v236
	v_and_b32_e32 v239, 0xffff0000, v236
	v_lshlrev_b32_e32 v240, 16, v237
	v_and_b32_e32 v241, 0xffff0000, v237
	v_mul_f32_e32 v238, s11, v238
	v_mul_f32_e32 v239, s11, v239
	v_mul_f32_e32 v240, s11, v240
	v_mul_f32_e32 v241, s11, v241
	v_med3_f32 v238, v238, s12, v215
	v_med3_f32 v239, v239, s12, v215
	v_med3_f32 v240, v240, s12, v215
	v_med3_f32 v241, v241, s12, v215
	v_add_f32_e32 v238, v216, v238
	v_add_f32_e32 v239, v216, v239
	v_add_f32_e32 v240, v216, v240
	v_add_f32_e32 v241, v216, v241
	v_perm_b32 v238, v239, v238, s24
	v_perm_b32 v240, v241, v240, s24
	v_lshl_or_b32 v249, v240, 16, v238
	global_store_dwordx2 v214, v[248:249], s[8:9] offset:32
	s_sub_u32 s8, s8, 0xbfc0
	s_subb_u32 s9, s9, 0
	s_mul_i32 s26, s25, 48
	s_add_u32 s6, s22, s26
	s_addc_u32 s7, s23, 0
	s_waitcnt vmcnt(39)
	v_cvt_pk_bf16_f32 v220, v0, v1
	v_cvt_pk_bf16_f32 v221, v2, v3
	ds_write_b64 v212, v[220:221] offset:0
	global_load_dwordx4 v[0:3], v211, s[6:7] offset:0 nt
	s_add_u32 s6, s6, s25
	s_addc_u32 s7, s7, 0
	s_waitcnt vmcnt(39)
	v_cvt_pk_bf16_f32 v220, v4, v5
	v_cvt_pk_bf16_f32 v221, v6, v7
	ds_write_b64 v212, v[220:221] offset:544
	global_load_dwordx4 v[4:7], v211, s[6:7] offset:0 nt
	s_add_u32 s6, s6, s25
	s_addc_u32 s7, s7, 0
	s_waitcnt vmcnt(39)
	v_cvt_pk_bf16_f32 v220, v8, v9
	v_cvt_pk_bf16_f32 v221, v10, v11
	ds_write_b64 v212, v[220:221] offset:1088
	global_load_dwordx4 v[8:11], v211, s[6:7] offset:0 nt
	s_add_u32 s6, s6, s25
	s_addc_u32 s7, s7, 0
	s_waitcnt vmcnt(39)
	v_cvt_pk_bf16_f32 v220, v12, v13
	v_cvt_pk_bf16_f32 v221, v14, v15
	ds_write_b64 v212, v[220:221] offset:1632
	global_load_dwordx4 v[12:15], v211, s[6:7] offset:0 nt
	s_add_u32 s6, s6, s25
	s_addc_u32 s7, s7, 0
	s_waitcnt vmcnt(39)
	v_cvt_pk_bf16_f32 v220, v16, v17
	v_cvt_pk_bf16_f32 v221, v18, v19
	ds_write_b64 v212, v[220:221] offset:2176
	global_load_dwordx4 v[16:19], v211, s[6:7] offset:0 nt
	s_add_u32 s6, s6, s25
	s_addc_u32 s7, s7, 0
	s_waitcnt vmcnt(39)
	v_cvt_pk_bf16_f32 v220, v20, v21
	v_cvt_pk_bf16_f32 v221, v22, v23
	ds_write_b64 v212, v[220:221] offset:2720
	global_load_dwordx4 v[20:23], v211, s[6:7] offset:0 nt
	s_add_u32 s6, s6, s25
	s_addc_u32 s7, s7, 0
	s_waitcnt vmcnt(39)
; #define LAS __attribute__((address_space(3)))
; #define LDS_WAIT() asm volatile("s_waitcnt lgkmcnt(0)" ::: "memory")
; __device__ __forceinline__ unsigned pk2(float lo, float hi) { return f2bf(lo) | (f2bf(hi) << 16); }
; __device__ __forceinline__ unsigned q8x4(float a, float b, float c, float d, float s) { return q8_(a, s) | (q8_(b, s) << 8) | (q8_(c, s) << 16) | (q8_(d, s) << 24); }
;     ...
;     for (int i = 0; i < 16; ++i) { vv[i] = (f32x4){0.f, 0.f, 0.f, 0.f}; if (okn) vv[i] = __builtin_nontemporal_load((const f32x4*)(wp + (size_t)(4 * i) * ldw)); }
; #pragma unroll
;     for (int i = 0; i < 16; ++i) { v2u w2; w2.x = pk2(vv[i][0], vv[i][1]); w2.y = pk2(vv[i][2], vv[i][3]); *(LAS v2u*)(scr + (4 * i + g) * 136 + nn * 2) = w2; }
;     LDS_WAIT(); asm volatile("" ::: "memory");
;     const int i16 = lane & 15, q = i16 >> 2, p = i16 & 3;
; #pragma unroll
;     for (int s = 0; s < 8; ++s) { const int nbk = s & 3, kbk = 4 * (s >> 2) + g;
;         const v4i16_t lo = __builtin_amdgcn_ds_read_tr16_b64_v4i16((LAS v4i16_t*)(scr + (8 * kbk + q) * 136 + 32 * nbk + 8 * p));
;         const v4i16_t hi = __builtin_amdgcn_ds_read_tr16_b64_v4i16((LAS v4i16_t*)(scr + (8 * kbk + 4 + q) * 136 + 32 * nbk + 8 * p));
;         const bf16x8 o = __builtin_shufflevector(lo, hi, 0, 1, 2, 3, 4, 5, 6, 7); const int n = 16 * nbk + i16;
;         if (n0 + n < nc) {
;             if constexpr (QMODE == 0) *(bf16x8*)(WT + (size_t)(r0 + n0 + n) * K + k0 + 8 * kbk) = o;
;             else { const v4u ou = __builtin_bit_cast(v4u, o); const float sc_ = QMODE == 1 ? QS_WUP : (QMODE == 2 ? QS_WDN : QS_WIN);
;                 *(v2u*)((unsigned char*)WT + (size_t)(r0 + n0 + n) * K + k0 + 8 * kbk) = (v2u){q8x4(bflo(ou.x), bfhi(ou.x), bflo(ou.y), bfhi(ou.y), sc_), q8x4(bflo(ou.z), bfhi(ou.z), bflo(ou.w), bfhi(ou.w), sc_)}; } } }
	v_cvt_pk_bf16_f32 v220, v24, v25
	v_cvt_pk_bf16_f32 v221, v26, v27
	ds_write_b64 v212, v[220:221] offset:3264
	global_load_dwordx4 v[24:27], v211, s[6:7] offset:0 nt
	s_add_u32 s6, s6, s25
	s_addc_u32 s7, s7, 0
	s_waitcnt vmcnt(39)
	v_cvt_pk_bf16_f32 v220, v28, v29
	v_cvt_pk_bf16_f32 v221, v30, v31
	ds_write_b64 v212, v[220:221] offset:3808
	global_load_dwordx4 v[28:31], v211, s[6:7] offset:0 nt
	s_add_u32 s6, s6, s25
	s_addc_u32 s7, s7, 0
	s_waitcnt vmcnt(39)
	v_cvt_pk_bf16_f32 v220, v32, v33
	v_cvt_pk_bf16_f32 v221, v34, v35
	ds_write_b64 v212, v[220:221] offset:4352
	global_load_dwordx4 v[32:35], v211, s[6:7] offset:0 nt
	s_add_u32 s6, s6, s25
	s_addc_u32 s7, s7, 0
	s_waitcnt vmcnt(39)
	v_cvt_pk_bf16_f32 v220, v36, v37
	v_cvt_pk_bf16_f32 v221, v38, v39
	ds_write_b64 v212, v[220:221] offset:4896
	global_load_dwordx4 v[36:39], v211, s[6:7] offset:0 nt
	s_add_u32 s6, s6, s25
	s_addc_u32 s7, s7, 0
	s_waitcnt vmcnt(39)
	v_cvt_pk_bf16_f32 v220, v40, v41
	v_cvt_pk_bf16_f32 v221, v42, v43
	ds_write_b64 v212, v[220:221] offset:5440
	s_waitcnt lgkmcnt(8)
	global_load_dwordx4 v[40:43], v211, s[6:7] offset:0 nt
	s_add_u32 s6, s6, s25
	s_addc_u32 s7, s7, 0
	s_waitcnt vmcnt(39)
	v_cvt_pk_bf16_f32 v220, v44, v45
	v_cvt_pk_bf16_f32 v221, v46, v47
	ds_write_b64 v212, v[220:221] offset:5984
	s_waitcnt lgkmcnt(8)
	global_load_dwordx4 v[44:47], v211, s[6:7] offset:0 nt
	s_add_u32 s6, s6, s25
	s_addc_u32 s7, s7, 0
	s_waitcnt vmcnt(39)
	v_cvt_pk_bf16_f32 v220, v48, v49
	v_cvt_pk_bf16_f32 v221, v50, v51
	ds_write_b64 v212, v[220:221] offset:6528
	s_waitcnt lgkmcnt(8)
	global_load_dwordx4 v[48:51], v211, s[6:7] offset:0 nt
	s_add_u32 s6, s6, s25
	s_addc_u32 s7, s7, 0
	s_waitcnt vmcnt(39)
	v_cvt_pk_bf16_f32 v220, v52, v53
	v_cvt_pk_bf16_f32 v221, v54, v55
	ds_write_b64 v212, v[220:221] offset:7072
	s_waitcnt lgkmcnt(8)
	global_load_dwordx4 v[52:55], v211, s[6:7] offset:0 nt
	s_add_u32 s6, s6, s25
	s_addc_u32 s7, s7, 0
	s_waitcnt vmcnt(39)
	v_cvt_pk_bf16_f32 v220, v56, v57
	v_cvt_pk_bf16_f32 v221, v58, v59
	ds_write_b64 v212, v[220:221] offset:7616
	s_waitcnt lgkmcnt(8)
	global_load_dwordx4 v[56:59], v211, s[6:7] offset:0 nt
	s_add_u32 s6, s6, s25
	s_addc_u32 s7, s7, 0
	s_waitcnt vmcnt(39)
	v_cvt_pk_bf16_f32 v220, v60, v61
	v_cvt_pk_bf16_f32 v221, v62, v63
	ds_write_b64 v212, v[220:221] offset:8160
	global_load_dwordx4 v[60:63], v211, s[6:7] offset:0 nt
	s_waitcnt lgkmcnt(0)
	ds_read_b64_tr_b16 v[222:223], v213 offset:0
	ds_read_b64_tr_b16 v[224:225], v213 offset:544
	ds_read_b64_tr_b16 v[226:227], v213 offset:4352
	ds_read_b64_tr_b16 v[228:229], v213 offset:4896
	ds_read_b64_tr_b16 v[230:231], v213 offset:32
	ds_read_b64_tr_b16 v[232:233], v213 offset:576
	ds_read_b64_tr_b16 v[234:235], v213 offset:4384
	ds_read_b64_tr_b16 v[236:237], v213 offset:4928
	s_waitcnt lgkmcnt(6)
	v_lshlrev_b32_e32 v238, 16, v222
	v_and_b32_e32 v239, 0xffff0000, v222
	v_lshlrev_b32_e32 v240, 16, v223
	v_and_b32_e32 v241, 0xffff0000, v223
	v_mul_f32_e32 v238, s11, v238
	v_mul_f32_e32 v239, s11, v239
	v_mul_f32_e32 v240, s11, v240
	v_mul_f32_e32 v241, s11, v241
	v_med3_f32 v238, v238, s12, v215
	v_med3_f32 v239, v239, s12, v215
	v_med3_f32 v240, v240, s12, v215
	v_med3_f32 v241, v241, s12, v215
	v_add_f32_e32 v238, v216, v238
	v_add_f32_e32 v239, v216, v239
	v_add_f32_e32 v240, v216, v240
	v_add_f32_e32 v241, v216, v241
	v_perm_b32 v238, v239, v238, s24
	v_perm_b32 v240, v241, v240, s24
	v_lshl_or_b32 v246, v240, 16, v238
	v_lshlrev_b32_e32 v238, 16, v224
	v_and_b32_e32 v239, 0xffff0000, v224
	v_lshlrev_b32_e32 v240, 16, v225
	v_and_b32_e32 v241, 0xffff0000, v225
	v_mul_f32_e32 v238, s11, v238
	v_mul_f32_e32 v239, s11, v239
	v_mul_f32_e32 v240, s11, v240
	v_mul_f32_e32 v241, s11, v241
	v_med3_f32 v238, v238, s12, v215
	v_med3_f32 v239, v239, s12, v215
	v_med3_f32 v240, v240, s12, v215
	v_med3_f32 v241, v241, s12, v215
	v_add_f32_e32 v238, v216, v238
	v_add_f32_e32 v239, v216, v239
	v_add_f32_e32 v240, v216, v240
	v_add_f32_e32 v241, v216, v241
	v_perm_b32 v238, v239, v238, s24
	v_perm_b32 v240, v241, v240, s24
	v_lshl_or_b32 v247, v240, 16, v238
	global_store_dwordx2 v214, v[246:247], s[8:9]
	s_waitcnt lgkmcnt(4)
	v_lshlrev_b32_e32 v238, 16, v226
	v_and_b32_e32 v239, 0xffff0000, v226
	v_lshlrev_b32_e32 v240, 16, v227
	v_and_b32_e32 v241, 0xffff0000, v227
	v_mul_f32_e32 v238, s11, v238
	v_mul_f32_e32 v239, s11, v239
	v_mul_f32_e32 v240, s11, v240
	v_mul_f32_e32 v241, s11, v241
	v_med3_f32 v238, v238, s12, v215
	v_med3_f32 v239, v239, s12, v215
	v_med3_f32 v240, v240, s12, v215
	v_med3_f32 v241, v241, s12, v215
	v_add_f32_e32 v238, v216, v238
	v_add_f32_e32 v239, v216, v239
	v_add_f32_e32 v240, v216, v240
	v_add_f32_e32 v241, v216, v241
	v_perm_b32 v238, v239, v238, s24
	v_perm_b32 v240, v241, v240, s24
	v_lshl_or_b32 v248, v240, 16, v238
	v_lshlrev_b32_e32 v238, 16, v228
	v_and_b32_e32 v239, 0xffff0000, v228
	v_lshlrev_b32_e32 v240, 16, v229
	v_and_b32_e32 v241, 0xffff0000, v229
	v_mul_f32_e32 v238, s11, v238
	v_mul_f32_e32 v239, s11, v239
	v_mul_f32_e32 v240, s11, v240
	v_mul_f32_e32 v241, s11, v241
	v_med3_f32 v238, v238, s12, v215
	v_med3_f32 v239, v239, s12, v215
	v_med3_f32 v240, v240, s12, v215
	v_med3_f32 v241, v241, s12, v215
	v_add_f32_e32 v238, v216, v238
	v_add_f32_e32 v239, v216, v239
	v_add_f32_e32 v240, v216, v240
	v_add_f32_e32 v241, v216, v241
	v_perm_b32 v238, v239, v238, s24
	v_perm_b32 v240, v241, v240, s24
	v_lshl_or_b32 v249, v240, 16, v238
	global_store_dwordx2 v214, v[248:249], s[8:9] offset:32
	ds_read_b64_tr_b16 v[222:223], v213 offset:64
	ds_read_b64_tr_b16 v[224:225], v213 offset:608
	ds_read_b64_tr_b16 v[226:227], v213 offset:4416
	ds_read_b64_tr_b16 v[228:229], v213 offset:4960
	s_add_u32 s8, s8, 0x4000
	s_addc_u32 s9, s9, 0
	s_waitcnt lgkmcnt(6)
; #define LAS __attribute__((address_space(3)))
; __device__ __forceinline__ unsigned q8x4(float a, float b, float c, float d, float s) { return q8_(a, s) | (q8_(b, s) << 8) | (q8_(c, s) << 16) | (q8_(d, s) << 24); }
;     ...
;     const int i16 = lane & 15, q = i16 >> 2, p = i16 & 3;
; #pragma unroll
;     for (int s = 0; s < 8; ++s) { const int nbk = s & 3, kbk = 4 * (s >> 2) + g;
;         const v4i16_t lo = __builtin_amdgcn_ds_read_tr16_b64_v4i16((LAS v4i16_t*)(scr + (8 * kbk + q) * 136 + 32 * nbk + 8 * p));
;         const v4i16_t hi = __builtin_amdgcn_ds_read_tr16_b64_v4i16((LAS v4i16_t*)(scr + (8 * kbk + 4 + q) * 136 + 32 * nbk + 8 * p));
;         const bf16x8 o = __builtin_shufflevector(lo, hi, 0, 1, 2, 3, 4, 5, 6, 7); const int n = 16 * nbk + i16;
;         if (n0 + n < nc) {
;             if constexpr (QMODE == 0) *(bf16x8*)(WT + (size_t)(r0 + n0 + n) * K + k0 + 8 * kbk) = o;
;             else { const v4u ou = __builtin_bit_cast(v4u, o); const float sc_ = QMODE == 1 ? QS_WUP : (QMODE == 2 ? QS_WDN : QS_WIN);
;                 *(v2u*)((unsigned char*)WT + (size_t)(r0 + n0 + n) * K + k0 + 8 * kbk) = (v2u){q8x4(bflo(ou.x), bfhi(ou.x), bflo(ou.y), bfhi(ou.y), sc_), q8x4(bflo(ou.z), bfhi(ou.z), bflo(ou.w), bfhi(ou.w), sc_)}; } } }
	v_lshlrev_b32_e32 v238, 16, v230
	v_and_b32_e32 v239, 0xffff0000, v230
	v_lshlrev_b32_e32 v240, 16, v231
	v_and_b32_e32 v241, 0xffff0000, v231
	v_mul_f32_e32 v238, s11, v238
	v_mul_f32_e32 v239, s11, v239
	v_mul_f32_e32 v240, s11, v240
	v_mul_f32_e32 v241, s11, v241
	v_med3_f32 v238, v238, s12, v215
	v_med3_f32 v239, v239, s12, v215
	v_med3_f32 v240, v240, s12, v215
	v_med3_f32 v241, v241, s12, v215
	v_add_f32_e32 v238, v216, v238
	v_add_f32_e32 v239, v216, v239
	v_add_f32_e32 v240, v216, v240
	v_add_f32_e32 v241, v216, v241
	v_perm_b32 v238, v239, v238, s24
	v_perm_b32 v240, v241, v240, s24
	v_lshl_or_b32 v246, v240, 16, v238
	v_lshlrev_b32_e32 v238, 16, v232
	v_and_b32_e32 v239, 0xffff0000, v232
	v_lshlrev_b32_e32 v240, 16, v233
	v_and_b32_e32 v241, 0xffff0000, v233
	v_mul_f32_e32 v238, s11, v238
	v_mul_f32_e32 v239, s11, v239
	v_mul_f32_e32 v240, s11, v240
	v_mul_f32_e32 v241, s11, v241
	v_med3_f32 v238, v238, s12, v215
	v_med3_f32 v239, v239, s12, v215
	v_med3_f32 v240, v240, s12, v215
	v_med3_f32 v241, v241, s12, v215
	v_add_f32_e32 v238, v216, v238
	v_add_f32_e32 v239, v216, v239
	v_add_f32_e32 v240, v216, v240
	v_add_f32_e32 v241, v216, v241
	v_perm_b32 v238, v239, v238, s24
	v_perm_b32 v240, v241, v240, s24
	v_lshl_or_b32 v247, v240, 16, v238
	global_store_dwordx2 v214, v[246:247], s[8:9]
	s_waitcnt lgkmcnt(4)
	v_lshlrev_b32_e32 v238, 16, v234
	v_and_b32_e32 v239, 0xffff0000, v234
	v_lshlrev_b32_e32 v240, 16, v235
	v_and_b32_e32 v241, 0xffff0000, v235
	v_mul_f32_e32 v238, s11, v238
	v_mul_f32_e32 v239, s11, v239
	v_mul_f32_e32 v240, s11, v240
	v_mul_f32_e32 v241, s11, v241
	v_med3_f32 v238, v238, s12, v215
	v_med3_f32 v239, v239, s12, v215
	v_med3_f32 v240, v240, s12, v215
	v_med3_f32 v241, v241, s12, v215
	v_add_f32_e32 v238, v216, v238
	v_add_f32_e32 v239, v216, v239
	v_add_f32_e32 v240, v216, v240
	v_add_f32_e32 v241, v216, v241
	v_perm_b32 v238, v239, v238, s24
	v_perm_b32 v240, v241, v240, s24
	v_lshl_or_b32 v248, v240, 16, v238
	v_lshlrev_b32_e32 v238, 16, v236
	v_and_b32_e32 v239, 0xffff0000, v236
	v_lshlrev_b32_e32 v240, 16, v237
	v_and_b32_e32 v241, 0xffff0000, v237
	v_mul_f32_e32 v238, s11, v238
	v_mul_f32_e32 v239, s11, v239
	v_mul_f32_e32 v240, s11, v240
	v_mul_f32_e32 v241, s11, v241
	v_med3_f32 v238, v238, s12, v215
	v_med3_f32 v239, v239, s12, v215
	v_med3_f32 v240, v240, s12, v215
	v_med3_f32 v241, v241, s12, v215
	v_add_f32_e32 v238, v216, v238
	v_add_f32_e32 v239, v216, v239
	v_add_f32_e32 v240, v216, v240
	v_add_f32_e32 v241, v216, v241
	v_perm_b32 v238, v239, v238, s24
	v_perm_b32 v240, v241, v240, s24
	v_lshl_or_b32 v249, v240, 16, v238
	global_store_dwordx2 v214, v[248:249], s[8:9] offset:32
	ds_read_b64_tr_b16 v[230:231], v213 offset:96
	ds_read_b64_tr_b16 v[232:233], v213 offset:640
	ds_read_b64_tr_b16 v[234:235], v213 offset:4448
	ds_read_b64_tr_b16 v[236:237], v213 offset:4992
	s_add_u32 s8, s8, 0x4000
	s_addc_u32 s9, s9, 0
	s_waitcnt lgkmcnt(6)
	v_lshlrev_b32_e32 v238, 16, v222
	v_and_b32_e32 v239, 0xffff0000, v222
	v_lshlrev_b32_e32 v240, 16, v223
	v_and_b32_e32 v241, 0xffff0000, v223
	v_mul_f32_e32 v238, s11, v238
	v_mul_f32_e32 v239, s11, v239
	v_mul_f32_e32 v240, s11, v240
	v_mul_f32_e32 v241, s11, v241
	v_med3_f32 v238, v238, s12, v215
	v_med3_f32 v239, v239, s12, v215
	v_med3_f32 v240, v240, s12, v215
	v_med3_f32 v241, v241, s12, v215
	v_add_f32_e32 v238, v216, v238
	v_add_f32_e32 v239, v216, v239
	v_add_f32_e32 v240, v216, v240
	v_add_f32_e32 v241, v216, v241
	v_perm_b32 v238, v239, v238, s24
	v_perm_b32 v240, v241, v240, s24
	v_lshl_or_b32 v246, v240, 16, v238
	v_lshlrev_b32_e32 v238, 16, v224
	v_and_b32_e32 v239, 0xffff0000, v224
	v_lshlrev_b32_e32 v240, 16, v225
	v_and_b32_e32 v241, 0xffff0000, v225
	v_mul_f32_e32 v238, s11, v238
	v_mul_f32_e32 v239, s11, v239
	v_mul_f32_e32 v240, s11, v240
	v_mul_f32_e32 v241, s11, v241
	v_med3_f32 v238, v238, s12, v215
	v_med3_f32 v239, v239, s12, v215
	v_med3_f32 v240, v240, s12, v215
	v_med3_f32 v241, v241, s12, v215
	v_add_f32_e32 v238, v216, v238
	v_add_f32_e32 v239, v216, v239
	v_add_f32_e32 v240, v216, v240
	v_add_f32_e32 v241, v216, v241
	v_perm_b32 v238, v239, v238, s24
	v_perm_b32 v240, v241, v240, s24
	v_lshl_or_b32 v247, v240, 16, v238
	global_store_dwordx2 v214, v[246:247], s[8:9]
	s_waitcnt lgkmcnt(4)
	v_lshlrev_b32_e32 v238, 16, v226
	v_and_b32_e32 v239, 0xffff0000, v226
	v_lshlrev_b32_e32 v240, 16, v227
	v_and_b32_e32 v241, 0xffff0000, v227
	v_mul_f32_e32 v238, s11, v238
	v_mul_f32_e32 v239, s11, v239
	v_mul_f32_e32 v240, s11, v240
	v_mul_f32_e32 v241, s11, v241
	v_med3_f32 v238, v238, s12, v215
	v_med3_f32 v239, v239, s12, v215
	v_med3_f32 v240, v240, s12, v215
	v_med3_f32 v241, v241, s12, v215
	v_add_f32_e32 v238, v216, v238
	v_add_f32_e32 v239, v216, v239
	v_add_f32_e32 v240, v216, v240
	v_add_f32_e32 v241, v216, v241
	v_perm_b32 v238, v239, v238, s24
	v_perm_b32 v240, v241, v240, s24
	v_lshl_or_b32 v248, v240, 16, v238
	v_lshlrev_b32_e32 v238, 16, v228
	v_and_b32_e32 v239, 0xffff0000, v228
	v_lshlrev_b32_e32 v240, 16, v229
	v_and_b32_e32 v241, 0xffff0000, v229
	v_mul_f32_e32 v238, s11, v238
	v_mul_f32_e32 v239, s11, v239
	v_mul_f32_e32 v240, s11, v240
	v_mul_f32_e32 v241, s11, v241
	v_med3_f32 v238, v238, s12, v215
	v_med3_f32 v239, v239, s12, v215
	v_med3_f32 v240, v240, s12, v215
	v_med3_f32 v241, v241, s12, v215
	v_add_f32_e32 v238, v216, v238
	v_add_f32_e32 v239, v216, v239
	v_add_f32_e32 v240, v216, v240
	v_add_f32_e32 v241, v216, v241
	v_perm_b32 v238, v239, v238, s24
	v_perm_b32 v240, v241, v240, s24
	v_lshl_or_b32 v249, v240, 16, v238
	global_store_dwordx2 v214, v[248:249], s[8:9] offset:32
	s_add_u32 s8, s8, 0x4000
	s_addc_u32 s9, s9, 0
	s_waitcnt lgkmcnt(2)
; #define LAS __attribute__((address_space(3)))
; __device__ __forceinline__ unsigned pk2(float lo, float hi) { return f2bf(lo) | (f2bf(hi) << 16); }
; __device__ __forceinline__ unsigned q8x4(float a, float b, float c, float d, float s) { return q8_(a, s) | (q8_(b, s) << 8) | (q8_(c, s) << 16) | (q8_(d, s) << 24); }
;     ...
;     for (int i = 0; i < 16; ++i) { vv[i] = (f32x4){0.f, 0.f, 0.f, 0.f}; if (okn) vv[i] = __builtin_nontemporal_load((const f32x4*)(wp + (size_t)(4 * i) * ldw)); }
; #pragma unroll
;     for (int i = 0; i < 16; ++i) { v2u w2; w2.x = pk2(vv[i][0], vv[i][1]); w2.y = pk2(vv[i][2], vv[i][3]); *(LAS v2u*)(scr + (4 * i + g) * 136 + nn * 2) = w2; }
;     ...
;     const int i16 = lane & 15, q = i16 >> 2, p = i16 & 3;
; #pragma unroll
;     for (int s = 0; s < 8; ++s) { const int nbk = s & 3, kbk = 4 * (s >> 2) + g;
;         const v4i16_t lo = __builtin_amdgcn_ds_read_tr16_b64_v4i16((LAS v4i16_t*)(scr + (8 * kbk + q) * 136 + 32 * nbk + 8 * p));
;         const v4i16_t hi = __builtin_amdgcn_ds_read_tr16_b64_v4i16((LAS v4i16_t*)(scr + (8 * kbk + 4 + q) * 136 + 32 * nbk + 8 * p));
;         const bf16x8 o = __builtin_shufflevector(lo, hi, 0, 1, 2, 3, 4, 5, 6, 7); const int n = 16 * nbk + i16;
;         if (n0 + n < nc) {
;             if constexpr (QMODE == 0) *(bf16x8*)(WT + (size_t)(r0 + n0 + n) * K + k0 + 8 * kbk) = o;
;             else { const v4u ou = __builtin_bit_cast(v4u, o); const float sc_ = QMODE == 1 ? QS_WUP : (QMODE == 2 ? QS_WDN : QS_WIN);
;                 *(v2u*)((unsigned char*)WT + (size_t)(r0 + n0 + n) * K + k0 + 8 * kbk) = (v2u){q8x4(bflo(ou.x), bfhi(ou.x), bflo(ou.y), bfhi(ou.y), sc_), q8x4(bflo(ou.z), bfhi(ou.z), bflo(ou.w), bfhi(ou.w), sc_)}; } } }
	v_lshlrev_b32_e32 v238, 16, v230
	v_and_b32_e32 v239, 0xffff0000, v230
	v_lshlrev_b32_e32 v240, 16, v231
	v_and_b32_e32 v241, 0xffff0000, v231
	v_mul_f32_e32 v238, s11, v238
	v_mul_f32_e32 v239, s11, v239
	v_mul_f32_e32 v240, s11, v240
	v_mul_f32_e32 v241, s11, v241
	v_med3_f32 v238, v238, s12, v215
	v_med3_f32 v239, v239, s12, v215
	v_med3_f32 v240, v240, s12, v215
	v_med3_f32 v241, v241, s12, v215
	v_add_f32_e32 v238, v216, v238
	v_add_f32_e32 v239, v216, v239
	v_add_f32_e32 v240, v216, v240
	v_add_f32_e32 v241, v216, v241
	v_perm_b32 v238, v239, v238, s24
	v_perm_b32 v240, v241, v240, s24
	v_lshl_or_b32 v246, v240, 16, v238
	v_lshlrev_b32_e32 v238, 16, v232
	v_and_b32_e32 v239, 0xffff0000, v232
	v_lshlrev_b32_e32 v240, 16, v233
	v_and_b32_e32 v241, 0xffff0000, v233
	v_mul_f32_e32 v238, s11, v238
	v_mul_f32_e32 v239, s11, v239
	v_mul_f32_e32 v240, s11, v240
	v_mul_f32_e32 v241, s11, v241
	v_med3_f32 v238, v238, s12, v215
	v_med3_f32 v239, v239, s12, v215
	v_med3_f32 v240, v240, s12, v215
	v_med3_f32 v241, v241, s12, v215
	v_add_f32_e32 v238, v216, v238
	v_add_f32_e32 v239, v216, v239
	v_add_f32_e32 v240, v216, v240
	v_add_f32_e32 v241, v216, v241
	v_perm_b32 v238, v239, v238, s24
	v_perm_b32 v240, v241, v240, s24
	v_lshl_or_b32 v247, v240, 16, v238
	global_store_dwordx2 v214, v[246:247], s[8:9]
	s_waitcnt lgkmcnt(0)
	v_lshlrev_b32_e32 v238, 16, v234
	v_and_b32_e32 v239, 0xffff0000, v234
	v_lshlrev_b32_e32 v240, 16, v235
	v_and_b32_e32 v241, 0xffff0000, v235
	v_mul_f32_e32 v238, s11, v238
	v_mul_f32_e32 v239, s11, v239
	v_mul_f32_e32 v240, s11, v240
	v_mul_f32_e32 v241, s11, v241
	v_med3_f32 v238, v238, s12, v215
	v_med3_f32 v239, v239, s12, v215
	v_med3_f32 v240, v240, s12, v215
	v_med3_f32 v241, v241, s12, v215
	v_add_f32_e32 v238, v216, v238
	v_add_f32_e32 v239, v216, v239
	v_add_f32_e32 v240, v216, v240
	v_add_f32_e32 v241, v216, v241
	v_perm_b32 v238, v239, v238, s24
	v_perm_b32 v240, v241, v240, s24
	v_lshl_or_b32 v248, v240, 16, v238
	v_lshlrev_b32_e32 v238, 16, v236
	v_and_b32_e32 v239, 0xffff0000, v236
	v_lshlrev_b32_e32 v240, 16, v237
	v_and_b32_e32 v241, 0xffff0000, v237
	v_mul_f32_e32 v238, s11, v238
	v_mul_f32_e32 v239, s11, v239
	v_mul_f32_e32 v240, s11, v240
	v_mul_f32_e32 v241, s11, v241
	v_med3_f32 v238, v238, s12, v215
	v_med3_f32 v239, v239, s12, v215
	v_med3_f32 v240, v240, s12, v215
	v_med3_f32 v241, v241, s12, v215
	v_add_f32_e32 v238, v216, v238
	v_add_f32_e32 v239, v216, v239
	v_add_f32_e32 v240, v216, v240
	v_add_f32_e32 v241, v216, v241
	v_perm_b32 v238, v239, v238, s24
	v_perm_b32 v240, v241, v240, s24
	v_lshl_or_b32 v249, v240, 16, v238
	global_store_dwordx2 v214, v[248:249], s[8:9] offset:32
	s_sub_u32 s8, s8, 0xbfc0
	s_subb_u32 s9, s9, 0
	s_waitcnt vmcnt(47)
	v_cvt_pk_bf16_f32 v220, v144, v145
	v_cvt_pk_bf16_f32 v221, v146, v147
	ds_write_b64 v212, v[220:221] offset:0
	s_waitcnt vmcnt(46)
	v_cvt_pk_bf16_f32 v220, v148, v149
	v_cvt_pk_bf16_f32 v221, v150, v151
	ds_write_b64 v212, v[220:221] offset:544
	s_waitcnt vmcnt(45)
	v_cvt_pk_bf16_f32 v220, v152, v153
	v_cvt_pk_bf16_f32 v221, v154, v155
	ds_write_b64 v212, v[220:221] offset:1088
	s_waitcnt vmcnt(44)
	v_cvt_pk_bf16_f32 v220, v156, v157
	v_cvt_pk_bf16_f32 v221, v158, v159
	ds_write_b64 v212, v[220:221] offset:1632
	s_waitcnt vmcnt(43)
	v_cvt_pk_bf16_f32 v220, v160, v161
	v_cvt_pk_bf16_f32 v221, v162, v163
	ds_write_b64 v212, v[220:221] offset:2176
	s_waitcnt vmcnt(42)
	v_cvt_pk_bf16_f32 v220, v164, v165
	v_cvt_pk_bf16_f32 v221, v166, v167
	ds_write_b64 v212, v[220:221] offset:2720
	s_waitcnt vmcnt(41)
	v_cvt_pk_bf16_f32 v220, v168, v169
	v_cvt_pk_bf16_f32 v221, v170, v171
	ds_write_b64 v212, v[220:221] offset:3264
	s_waitcnt vmcnt(40)
	v_cvt_pk_bf16_f32 v220, v172, v173
	v_cvt_pk_bf16_f32 v221, v174, v175
	ds_write_b64 v212, v[220:221] offset:3808
	s_waitcnt vmcnt(39)
	v_cvt_pk_bf16_f32 v220, v176, v177
	v_cvt_pk_bf16_f32 v221, v178, v179
	ds_write_b64 v212, v[220:221] offset:4352
	s_waitcnt vmcnt(38)
	v_cvt_pk_bf16_f32 v220, v180, v181
	v_cvt_pk_bf16_f32 v221, v182, v183
	ds_write_b64 v212, v[220:221] offset:4896
	s_waitcnt vmcnt(37)
	v_cvt_pk_bf16_f32 v220, v184, v185
	v_cvt_pk_bf16_f32 v221, v186, v187
	ds_write_b64 v212, v[220:221] offset:5440
	s_waitcnt lgkmcnt(8)
	s_waitcnt vmcnt(36)
	v_cvt_pk_bf16_f32 v220, v188, v189
	v_cvt_pk_bf16_f32 v221, v190, v191
	ds_write_b64 v212, v[220:221] offset:5984
	s_waitcnt lgkmcnt(8)
	s_waitcnt vmcnt(35)
	v_cvt_pk_bf16_f32 v220, v192, v193
	v_cvt_pk_bf16_f32 v221, v194, v195
	ds_write_b64 v212, v[220:221] offset:6528
	s_waitcnt lgkmcnt(8)
	s_waitcnt vmcnt(34)
	v_cvt_pk_bf16_f32 v220, v196, v197
	v_cvt_pk_bf16_f32 v221, v198, v199
	ds_write_b64 v212, v[220:221] offset:7072
	s_waitcnt lgkmcnt(8)
	s_waitcnt vmcnt(33)
	v_cvt_pk_bf16_f32 v220, v200, v201
	v_cvt_pk_bf16_f32 v221, v202, v203
	ds_write_b64 v212, v[220:221] offset:7616
	s_waitcnt lgkmcnt(8)
	s_waitcnt vmcnt(32)
	v_cvt_pk_bf16_f32 v220, v204, v205
	v_cvt_pk_bf16_f32 v221, v206, v207
	ds_write_b64 v212, v[220:221] offset:8160
	s_waitcnt lgkmcnt(0)
	ds_read_b64_tr_b16 v[222:223], v213 offset:0
	ds_read_b64_tr_b16 v[224:225], v213 offset:544
	ds_read_b64_tr_b16 v[226:227], v213 offset:4352
	ds_read_b64_tr_b16 v[228:229], v213 offset:4896
	ds_read_b64_tr_b16 v[230:231], v213 offset:32
	ds_read_b64_tr_b16 v[232:233], v213 offset:576
	ds_read_b64_tr_b16 v[234:235], v213 offset:4384
	ds_read_b64_tr_b16 v[236:237], v213 offset:4928
	s_waitcnt lgkmcnt(6)
; #define LAS __attribute__((address_space(3)))
; __device__ __forceinline__ unsigned q8x4(float a, float b, float c, float d, float s) { return q8_(a, s) | (q8_(b, s) << 8) | (q8_(c, s) << 16) | (q8_(d, s) << 24); }
;     ...
;     const int i16 = lane & 15, q = i16 >> 2, p = i16 & 3;
; #pragma unroll
;     for (int s = 0; s < 8; ++s) { const int nbk = s & 3, kbk = 4 * (s >> 2) + g;
;         const v4i16_t lo = __builtin_amdgcn_ds_read_tr16_b64_v4i16((LAS v4i16_t*)(scr + (8 * kbk + q) * 136 + 32 * nbk + 8 * p));
;         const v4i16_t hi = __builtin_amdgcn_ds_read_tr16_b64_v4i16((LAS v4i16_t*)(scr + (8 * kbk + 4 + q) * 136 + 32 * nbk + 8 * p));
;         const bf16x8 o = __builtin_shufflevector(lo, hi, 0, 1, 2, 3, 4, 5, 6, 7); const int n = 16 * nbk + i16;
;         if (n0 + n < nc) {
;             if constexpr (QMODE == 0) *(bf16x8*)(WT + (size_t)(r0 + n0 + n) * K + k0 + 8 * kbk) = o;
;             else { const v4u ou = __builtin_bit_cast(v4u, o); const float sc_ = QMODE == 1 ? QS_WUP : (QMODE == 2 ? QS_WDN : QS_WIN);
;                 *(v2u*)((unsigned char*)WT + (size_t)(r0 + n0 + n) * K + k0 + 8 * kbk) = (v2u){q8x4(bflo(ou.x), bfhi(ou.x), bflo(ou.y), bfhi(ou.y), sc_), q8x4(bflo(ou.z), bfhi(ou.z), bflo(ou.w), bfhi(ou.w), sc_)}; } } }
	v_lshlrev_b32_e32 v238, 16, v222
	v_and_b32_e32 v239, 0xffff0000, v222
	v_lshlrev_b32_e32 v240, 16, v223
	v_and_b32_e32 v241, 0xffff0000, v223
	v_mul_f32_e32 v238, s11, v238
	v_mul_f32_e32 v239, s11, v239
	v_mul_f32_e32 v240, s11, v240
	v_mul_f32_e32 v241, s11, v241
	v_med3_f32 v238, v238, s12, v215
	v_med3_f32 v239, v239, s12, v215
	v_med3_f32 v240, v240, s12, v215
	v_med3_f32 v241, v241, s12, v215
	v_add_f32_e32 v238, v216, v238
	v_add_f32_e32 v239, v216, v239
	v_add_f32_e32 v240, v216, v240
	v_add_f32_e32 v241, v216, v241
	v_perm_b32 v238, v239, v238, s24
	v_perm_b32 v240, v241, v240, s24
	v_lshl_or_b32 v246, v240, 16, v238
	v_lshlrev_b32_e32 v238, 16, v224
	v_and_b32_e32 v239, 0xffff0000, v224
	v_lshlrev_b32_e32 v240, 16, v225
	v_and_b32_e32 v241, 0xffff0000, v225
	v_mul_f32_e32 v238, s11, v238
	v_mul_f32_e32 v239, s11, v239
	v_mul_f32_e32 v240, s11, v240
	v_mul_f32_e32 v241, s11, v241
	v_med3_f32 v238, v238, s12, v215
	v_med3_f32 v239, v239, s12, v215
	v_med3_f32 v240, v240, s12, v215
	v_med3_f32 v241, v241, s12, v215
	v_add_f32_e32 v238, v216, v238
	v_add_f32_e32 v239, v216, v239
	v_add_f32_e32 v240, v216, v240
	v_add_f32_e32 v241, v216, v241
	v_perm_b32 v238, v239, v238, s24
	v_perm_b32 v240, v241, v240, s24
	v_lshl_or_b32 v247, v240, 16, v238
	global_store_dwordx2 v214, v[246:247], s[8:9]
	s_waitcnt lgkmcnt(4)
	v_lshlrev_b32_e32 v238, 16, v226
	v_and_b32_e32 v239, 0xffff0000, v226
	v_lshlrev_b32_e32 v240, 16, v227
	v_and_b32_e32 v241, 0xffff0000, v227
	v_mul_f32_e32 v238, s11, v238
	v_mul_f32_e32 v239, s11, v239
	v_mul_f32_e32 v240, s11, v240
	v_mul_f32_e32 v241, s11, v241
	v_med3_f32 v238, v238, s12, v215
	v_med3_f32 v239, v239, s12, v215
	v_med3_f32 v240, v240, s12, v215
	v_med3_f32 v241, v241, s12, v215
	v_add_f32_e32 v238, v216, v238
	v_add_f32_e32 v239, v216, v239
	v_add_f32_e32 v240, v216, v240
	v_add_f32_e32 v241, v216, v241
	v_perm_b32 v238, v239, v238, s24
	v_perm_b32 v240, v241, v240, s24
	v_lshl_or_b32 v248, v240, 16, v238
	v_lshlrev_b32_e32 v238, 16, v228
	v_and_b32_e32 v239, 0xffff0000, v228
	v_lshlrev_b32_e32 v240, 16, v229
	v_and_b32_e32 v241, 0xffff0000, v229
	v_mul_f32_e32 v238, s11, v238
	v_mul_f32_e32 v239, s11, v239
	v_mul_f32_e32 v240, s11, v240
	v_mul_f32_e32 v241, s11, v241
	v_med3_f32 v238, v238, s12, v215
	v_med3_f32 v239, v239, s12, v215
	v_med3_f32 v240, v240, s12, v215
	v_med3_f32 v241, v241, s12, v215
	v_add_f32_e32 v238, v216, v238
	v_add_f32_e32 v239, v216, v239
	v_add_f32_e32 v240, v216, v240
	v_add_f32_e32 v241, v216, v241
	v_perm_b32 v238, v239, v238, s24
	v_perm_b32 v240, v241, v240, s24
	v_lshl_or_b32 v249, v240, 16, v238
	global_store_dwordx2 v214, v[248:249], s[8:9] offset:32
	ds_read_b64_tr_b16 v[222:223], v213 offset:64
	ds_read_b64_tr_b16 v[224:225], v213 offset:608
	ds_read_b64_tr_b16 v[226:227], v213 offset:4416
	ds_read_b64_tr_b16 v[228:229], v213 offset:4960
	s_add_u32 s8, s8, 0x4000
	s_addc_u32 s9, s9, 0
	s_waitcnt lgkmcnt(6)
	v_lshlrev_b32_e32 v238, 16, v230
	v_and_b32_e32 v239, 0xffff0000, v230
	v_lshlrev_b32_e32 v240, 16, v231
	v_and_b32_e32 v241, 0xffff0000, v231
	v_mul_f32_e32 v238, s11, v238
	v_mul_f32_e32 v239, s11, v239
	v_mul_f32_e32 v240, s11, v240
	v_mul_f32_e32 v241, s11, v241
	v_med3_f32 v238, v238, s12, v215
	v_med3_f32 v239, v239, s12, v215
	v_med3_f32 v240, v240, s12, v215
	v_med3_f32 v241, v241, s12, v215
	v_add_f32_e32 v238, v216, v238
	v_add_f32_e32 v239, v216, v239
	v_add_f32_e32 v240, v216, v240
	v_add_f32_e32 v241, v216, v241
	v_perm_b32 v238, v239, v238, s24
	v_perm_b32 v240, v241, v240, s24
	v_lshl_or_b32 v246, v240, 16, v238
	v_lshlrev_b32_e32 v238, 16, v232
	v_and_b32_e32 v239, 0xffff0000, v232
	v_lshlrev_b32_e32 v240, 16, v233
	v_and_b32_e32 v241, 0xffff0000, v233
	v_mul_f32_e32 v238, s11, v238
	v_mul_f32_e32 v239, s11, v239
	v_mul_f32_e32 v240, s11, v240
	v_mul_f32_e32 v241, s11, v241
	v_med3_f32 v238, v238, s12, v215
	v_med3_f32 v239, v239, s12, v215
	v_med3_f32 v240, v240, s12, v215
	v_med3_f32 v241, v241, s12, v215
	v_add_f32_e32 v238, v216, v238
	v_add_f32_e32 v239, v216, v239
	v_add_f32_e32 v240, v216, v240
	v_add_f32_e32 v241, v216, v241
	v_perm_b32 v238, v239, v238, s24
	v_perm_b32 v240, v241, v240, s24
	v_lshl_or_b32 v247, v240, 16, v238
	global_store_dwordx2 v214, v[246:247], s[8:9]
	s_waitcnt lgkmcnt(4)
	v_lshlrev_b32_e32 v238, 16, v234
	v_and_b32_e32 v239, 0xffff0000, v234
	v_lshlrev_b32_e32 v240, 16, v235
	v_and_b32_e32 v241, 0xffff0000, v235
	v_mul_f32_e32 v238, s11, v238
	v_mul_f32_e32 v239, s11, v239
	v_mul_f32_e32 v240, s11, v240
	v_mul_f32_e32 v241, s11, v241
	v_med3_f32 v238, v238, s12, v215
	v_med3_f32 v239, v239, s12, v215
	v_med3_f32 v240, v240, s12, v215
	v_med3_f32 v241, v241, s12, v215
	v_add_f32_e32 v238, v216, v238
	v_add_f32_e32 v239, v216, v239
	v_add_f32_e32 v240, v216, v240
	v_add_f32_e32 v241, v216, v241
	v_perm_b32 v238, v239, v238, s24
	v_perm_b32 v240, v241, v240, s24
	v_lshl_or_b32 v248, v240, 16, v238
	v_lshlrev_b32_e32 v238, 16, v236
	v_and_b32_e32 v239, 0xffff0000, v236
	v_lshlrev_b32_e32 v240, 16, v237
	v_and_b32_e32 v241, 0xffff0000, v237
	v_mul_f32_e32 v238, s11, v238
	v_mul_f32_e32 v239, s11, v239
	v_mul_f32_e32 v240, s11, v240
	v_mul_f32_e32 v241, s11, v241
	v_med3_f32 v238, v238, s12, v215
	v_med3_f32 v239, v239, s12, v215
	v_med3_f32 v240, v240, s12, v215
	v_med3_f32 v241, v241, s12, v215
	v_add_f32_e32 v238, v216, v238
	v_add_f32_e32 v239, v216, v239
	v_add_f32_e32 v240, v216, v240
	v_add_f32_e32 v241, v216, v241
	v_perm_b32 v238, v239, v238, s24
	v_perm_b32 v240, v241, v240, s24
	v_lshl_or_b32 v249, v240, 16, v238
	global_store_dwordx2 v214, v[248:249], s[8:9] offset:32
	ds_read_b64_tr_b16 v[230:231], v213 offset:96
	ds_read_b64_tr_b16 v[232:233], v213 offset:640
	ds_read_b64_tr_b16 v[234:235], v213 offset:4448
	ds_read_b64_tr_b16 v[236:237], v213 offset:4992
	s_add_u32 s8, s8, 0x4000
	s_addc_u32 s9, s9, 0
	s_waitcnt lgkmcnt(6)
; #define LAS __attribute__((address_space(3)))
; __device__ __forceinline__ unsigned pk2(float lo, float hi) { return f2bf(lo) | (f2bf(hi) << 16); }
; __device__ __forceinline__ unsigned q8x4(float a, float b, float c, float d, float s) { return q8_(a, s) | (q8_(b, s) << 8) | (q8_(c, s) << 16) | (q8_(d, s) << 24); }
;     ...
;     for (int i = 0; i < 16; ++i) { vv[i] = (f32x4){0.f, 0.f, 0.f, 0.f}; if (okn) vv[i] = __builtin_nontemporal_load((const f32x4*)(wp + (size_t)(4 * i) * ldw)); }
; #pragma unroll
;     for (int i = 0; i < 16; ++i) { v2u w2; w2.x = pk2(vv[i][0], vv[i][1]); w2.y = pk2(vv[i][2], vv[i][3]); *(LAS v2u*)(scr + (4 * i + g) * 136 + nn * 2) = w2; }
;     ...
;     const int i16 = lane & 15, q = i16 >> 2, p = i16 & 3;
; #pragma unroll
;     for (int s = 0; s < 8; ++s) { const int nbk = s & 3, kbk = 4 * (s >> 2) + g;
;         const v4i16_t lo = __builtin_amdgcn_ds_read_tr16_b64_v4i16((LAS v4i16_t*)(scr + (8 * kbk + q) * 136 + 32 * nbk + 8 * p));
;         const v4i16_t hi = __builtin_amdgcn_ds_read_tr16_b64_v4i16((LAS v4i16_t*)(scr + (8 * kbk + 4 + q) * 136 + 32 * nbk + 8 * p));
;         const bf16x8 o = __builtin_shufflevector(lo, hi, 0, 1, 2, 3, 4, 5, 6, 7); const int n = 16 * nbk + i16;
;         if (n0 + n < nc) {
;             if constexpr (QMODE == 0) *(bf16x8*)(WT + (size_t)(r0 + n0 + n) * K + k0 + 8 * kbk) = o;
;             else { const v4u ou = __builtin_bit_cast(v4u, o); const float sc_ = QMODE == 1 ? QS_WUP : (QMODE == 2 ? QS_WDN : QS_WIN);
;                 *(v2u*)((unsigned char*)WT + (size_t)(r0 + n0 + n) * K + k0 + 8 * kbk) = (v2u){q8x4(bflo(ou.x), bfhi(ou.x), bflo(ou.y), bfhi(ou.y), sc_), q8x4(bflo(ou.z), bfhi(ou.z), bflo(ou.w), bfhi(ou.w), sc_)}; } } }
	v_lshlrev_b32_e32 v238, 16, v222
	v_and_b32_e32 v239, 0xffff0000, v222
	v_lshlrev_b32_e32 v240, 16, v223
	v_and_b32_e32 v241, 0xffff0000, v223
	v_mul_f32_e32 v238, s11, v238
	v_mul_f32_e32 v239, s11, v239
	v_mul_f32_e32 v240, s11, v240
	v_mul_f32_e32 v241, s11, v241
	v_med3_f32 v238, v238, s12, v215
	v_med3_f32 v239, v239, s12, v215
	v_med3_f32 v240, v240, s12, v215
	v_med3_f32 v241, v241, s12, v215
	v_add_f32_e32 v238, v216, v238
	v_add_f32_e32 v239, v216, v239
	v_add_f32_e32 v240, v216, v240
	v_add_f32_e32 v241, v216, v241
	v_perm_b32 v238, v239, v238, s24
	v_perm_b32 v240, v241, v240, s24
	v_lshl_or_b32 v246, v240, 16, v238
	v_lshlrev_b32_e32 v238, 16, v224
	v_and_b32_e32 v239, 0xffff0000, v224
	v_lshlrev_b32_e32 v240, 16, v225
	v_and_b32_e32 v241, 0xffff0000, v225
	v_mul_f32_e32 v238, s11, v238
	v_mul_f32_e32 v239, s11, v239
	v_mul_f32_e32 v240, s11, v240
	v_mul_f32_e32 v241, s11, v241
	v_med3_f32 v238, v238, s12, v215
	v_med3_f32 v239, v239, s12, v215
	v_med3_f32 v240, v240, s12, v215
	v_med3_f32 v241, v241, s12, v215
	v_add_f32_e32 v238, v216, v238
	v_add_f32_e32 v239, v216, v239
	v_add_f32_e32 v240, v216, v240
	v_add_f32_e32 v241, v216, v241
	v_perm_b32 v238, v239, v238, s24
	v_perm_b32 v240, v241, v240, s24
	v_lshl_or_b32 v247, v240, 16, v238
	global_store_dwordx2 v214, v[246:247], s[8:9]
	s_waitcnt lgkmcnt(4)
	v_lshlrev_b32_e32 v238, 16, v226
	v_and_b32_e32 v239, 0xffff0000, v226
	v_lshlrev_b32_e32 v240, 16, v227
	v_and_b32_e32 v241, 0xffff0000, v227
	v_mul_f32_e32 v238, s11, v238
	v_mul_f32_e32 v239, s11, v239
	v_mul_f32_e32 v240, s11, v240
	v_mul_f32_e32 v241, s11, v241
	v_med3_f32 v238, v238, s12, v215
	v_med3_f32 v239, v239, s12, v215
	v_med3_f32 v240, v240, s12, v215
	v_med3_f32 v241, v241, s12, v215
	v_add_f32_e32 v238, v216, v238
	v_add_f32_e32 v239, v216, v239
	v_add_f32_e32 v240, v216, v240
	v_add_f32_e32 v241, v216, v241
	v_perm_b32 v238, v239, v238, s24
	v_perm_b32 v240, v241, v240, s24
	v_lshl_or_b32 v248, v240, 16, v238
	v_lshlrev_b32_e32 v238, 16, v228
	v_and_b32_e32 v239, 0xffff0000, v228
	v_lshlrev_b32_e32 v240, 16, v229
	v_and_b32_e32 v241, 0xffff0000, v229
	v_mul_f32_e32 v238, s11, v238
	v_mul_f32_e32 v239, s11, v239
	v_mul_f32_e32 v240, s11, v240
	v_mul_f32_e32 v241, s11, v241
	v_med3_f32 v238, v238, s12, v215
	v_med3_f32 v239, v239, s12, v215
	v_med3_f32 v240, v240, s12, v215
	v_med3_f32 v241, v241, s12, v215
	v_add_f32_e32 v238, v216, v238
	v_add_f32_e32 v239, v216, v239
	v_add_f32_e32 v240, v216, v240
	v_add_f32_e32 v241, v216, v241
	v_perm_b32 v238, v239, v238, s24
	v_perm_b32 v240, v241, v240, s24
	v_lshl_or_b32 v249, v240, 16, v238
	global_store_dwordx2 v214, v[248:249], s[8:9] offset:32
	s_add_u32 s8, s8, 0x4000
	s_addc_u32 s9, s9, 0
	s_waitcnt lgkmcnt(2)
	v_lshlrev_b32_e32 v238, 16, v230
	v_and_b32_e32 v239, 0xffff0000, v230
	v_lshlrev_b32_e32 v240, 16, v231
	v_and_b32_e32 v241, 0xffff0000, v231
	v_mul_f32_e32 v238, s11, v238
	v_mul_f32_e32 v239, s11, v239
	v_mul_f32_e32 v240, s11, v240
	v_mul_f32_e32 v241, s11, v241
	v_med3_f32 v238, v238, s12, v215
	v_med3_f32 v239, v239, s12, v215
	v_med3_f32 v240, v240, s12, v215
	v_med3_f32 v241, v241, s12, v215
	v_add_f32_e32 v238, v216, v238
	v_add_f32_e32 v239, v216, v239
	v_add_f32_e32 v240, v216, v240
	v_add_f32_e32 v241, v216, v241
	v_perm_b32 v238, v239, v238, s24
	v_perm_b32 v240, v241, v240, s24
	v_lshl_or_b32 v246, v240, 16, v238
	v_lshlrev_b32_e32 v238, 16, v232
	v_and_b32_e32 v239, 0xffff0000, v232
	v_lshlrev_b32_e32 v240, 16, v233
	v_and_b32_e32 v241, 0xffff0000, v233
	v_mul_f32_e32 v238, s11, v238
	v_mul_f32_e32 v239, s11, v239
	v_mul_f32_e32 v240, s11, v240
	v_mul_f32_e32 v241, s11, v241
	v_med3_f32 v238, v238, s12, v215
	v_med3_f32 v239, v239, s12, v215
	v_med3_f32 v240, v240, s12, v215
	v_med3_f32 v241, v241, s12, v215
	v_add_f32_e32 v238, v216, v238
	v_add_f32_e32 v239, v216, v239
	v_add_f32_e32 v240, v216, v240
	v_add_f32_e32 v241, v216, v241
	v_perm_b32 v238, v239, v238, s24
	v_perm_b32 v240, v241, v240, s24
	v_lshl_or_b32 v247, v240, 16, v238
	global_store_dwordx2 v214, v[246:247], s[8:9]
	s_waitcnt lgkmcnt(0)
	v_lshlrev_b32_e32 v238, 16, v234
	v_and_b32_e32 v239, 0xffff0000, v234
	v_lshlrev_b32_e32 v240, 16, v235
	v_and_b32_e32 v241, 0xffff0000, v235
	v_mul_f32_e32 v238, s11, v238
	v_mul_f32_e32 v239, s11, v239
	v_mul_f32_e32 v240, s11, v240
	v_mul_f32_e32 v241, s11, v241
	v_med3_f32 v238, v238, s12, v215
	v_med3_f32 v239, v239, s12, v215
	v_med3_f32 v240, v240, s12, v215
	v_med3_f32 v241, v241, s12, v215
	v_add_f32_e32 v238, v216, v238
	v_add_f32_e32 v239, v216, v239
	v_add_f32_e32 v240, v216, v240
	v_add_f32_e32 v241, v216, v241
	v_perm_b32 v238, v239, v238, s24
	v_perm_b32 v240, v241, v240, s24
	v_lshl_or_b32 v248, v240, 16, v238
	v_lshlrev_b32_e32 v238, 16, v236
	v_and_b32_e32 v239, 0xffff0000, v236
	v_lshlrev_b32_e32 v240, 16, v237
	v_and_b32_e32 v241, 0xffff0000, v237
	v_mul_f32_e32 v238, s11, v238
	v_mul_f32_e32 v239, s11, v239
	v_mul_f32_e32 v240, s11, v240
	v_mul_f32_e32 v241, s11, v241
	v_med3_f32 v238, v238, s12, v215
	v_med3_f32 v239, v239, s12, v215
	v_med3_f32 v240, v240, s12, v215
	v_med3_f32 v241, v241, s12, v215
	v_add_f32_e32 v238, v216, v238
	v_add_f32_e32 v239, v216, v239
	v_add_f32_e32 v240, v216, v240
	v_add_f32_e32 v241, v216, v241
	v_perm_b32 v238, v239, v238, s24
	v_perm_b32 v240, v241, v240, s24
	v_lshl_or_b32 v249, v240, 16, v238
	global_store_dwordx2 v214, v[248:249], s[8:9] offset:32
	s_sub_u32 s8, s8, 0xbfc0
	s_subb_u32 s9, s9, 0
	s_waitcnt vmcnt(31)
	v_cvt_pk_bf16_f32 v220, v0, v1
	v_cvt_pk_bf16_f32 v221, v2, v3
	ds_write_b64 v212, v[220:221] offset:0
	s_waitcnt vmcnt(30)
; #define LAS __attribute__((address_space(3)))
; #define LDS_WAIT() asm volatile("s_waitcnt lgkmcnt(0)" ::: "memory")
; __device__ __forceinline__ unsigned pk2(float lo, float hi) { return f2bf(lo) | (f2bf(hi) << 16); }
; __device__ __forceinline__ unsigned q8x4(float a, float b, float c, float d, float s) { return q8_(a, s) | (q8_(b, s) << 8) | (q8_(c, s) << 16) | (q8_(d, s) << 24); }
;     ...
;     for (int i = 0; i < 16; ++i) { vv[i] = (f32x4){0.f, 0.f, 0.f, 0.f}; if (okn) vv[i] = __builtin_nontemporal_load((const f32x4*)(wp + (size_t)(4 * i) * ldw)); }
; #pragma unroll
;     for (int i = 0; i < 16; ++i) { v2u w2; w2.x = pk2(vv[i][0], vv[i][1]); w2.y = pk2(vv[i][2], vv[i][3]); *(LAS v2u*)(scr + (4 * i + g) * 136 + nn * 2) = w2; }
;     LDS_WAIT(); asm volatile("" ::: "memory");
;     const int i16 = lane & 15, q = i16 >> 2, p = i16 & 3;
; #pragma unroll
;     for (int s = 0; s < 8; ++s) { const int nbk = s & 3, kbk = 4 * (s >> 2) + g;
;         const v4i16_t lo = __builtin_amdgcn_ds_read_tr16_b64_v4i16((LAS v4i16_t*)(scr + (8 * kbk + q) * 136 + 32 * nbk + 8 * p));
;         const v4i16_t hi = __builtin_amdgcn_ds_read_tr16_b64_v4i16((LAS v4i16_t*)(scr + (8 * kbk + 4 + q) * 136 + 32 * nbk + 8 * p));
;         const bf16x8 o = __builtin_shufflevector(lo, hi, 0, 1, 2, 3, 4, 5, 6, 7); const int n = 16 * nbk + i16;
;         if (n0 + n < nc) {
;             if constexpr (QMODE == 0) *(bf16x8*)(WT + (size_t)(r0 + n0 + n) * K + k0 + 8 * kbk) = o;
;             else { const v4u ou = __builtin_bit_cast(v4u, o); const float sc_ = QMODE == 1 ? QS_WUP : (QMODE == 2 ? QS_WDN : QS_WIN);
;                 *(v2u*)((unsigned char*)WT + (size_t)(r0 + n0 + n) * K + k0 + 8 * kbk) = (v2u){q8x4(bflo(ou.x), bfhi(ou.x), bflo(ou.y), bfhi(ou.y), sc_), q8x4(bflo(ou.z), bfhi(ou.z), bflo(ou.w), bfhi(ou.w), sc_)}; } } }
	v_cvt_pk_bf16_f32 v220, v4, v5
	v_cvt_pk_bf16_f32 v221, v6, v7
	ds_write_b64 v212, v[220:221] offset:544
	s_waitcnt vmcnt(29)
	v_cvt_pk_bf16_f32 v220, v8, v9
	v_cvt_pk_bf16_f32 v221, v10, v11
	ds_write_b64 v212, v[220:221] offset:1088
	s_waitcnt vmcnt(28)
	v_cvt_pk_bf16_f32 v220, v12, v13
	v_cvt_pk_bf16_f32 v221, v14, v15
	ds_write_b64 v212, v[220:221] offset:1632
	s_waitcnt vmcnt(27)
	v_cvt_pk_bf16_f32 v220, v16, v17
	v_cvt_pk_bf16_f32 v221, v18, v19
	ds_write_b64 v212, v[220:221] offset:2176
	s_waitcnt vmcnt(26)
	v_cvt_pk_bf16_f32 v220, v20, v21
	v_cvt_pk_bf16_f32 v221, v22, v23
	ds_write_b64 v212, v[220:221] offset:2720
	s_waitcnt vmcnt(25)
	v_cvt_pk_bf16_f32 v220, v24, v25
	v_cvt_pk_bf16_f32 v221, v26, v27
	ds_write_b64 v212, v[220:221] offset:3264
	s_waitcnt vmcnt(24)
	v_cvt_pk_bf16_f32 v220, v28, v29
	v_cvt_pk_bf16_f32 v221, v30, v31
	ds_write_b64 v212, v[220:221] offset:3808
	s_waitcnt vmcnt(23)
	v_cvt_pk_bf16_f32 v220, v32, v33
	v_cvt_pk_bf16_f32 v221, v34, v35
	ds_write_b64 v212, v[220:221] offset:4352
	s_waitcnt vmcnt(22)
	v_cvt_pk_bf16_f32 v220, v36, v37
	v_cvt_pk_bf16_f32 v221, v38, v39
	ds_write_b64 v212, v[220:221] offset:4896
	s_waitcnt vmcnt(21)
	v_cvt_pk_bf16_f32 v220, v40, v41
	v_cvt_pk_bf16_f32 v221, v42, v43
	ds_write_b64 v212, v[220:221] offset:5440
	s_waitcnt lgkmcnt(8)
	s_waitcnt vmcnt(20)
	v_cvt_pk_bf16_f32 v220, v44, v45
	v_cvt_pk_bf16_f32 v221, v46, v47
	ds_write_b64 v212, v[220:221] offset:5984
	s_waitcnt lgkmcnt(8)
	s_waitcnt vmcnt(19)
	v_cvt_pk_bf16_f32 v220, v48, v49
	v_cvt_pk_bf16_f32 v221, v50, v51
	ds_write_b64 v212, v[220:221] offset:6528
	s_waitcnt lgkmcnt(8)
	s_waitcnt vmcnt(18)
	v_cvt_pk_bf16_f32 v220, v52, v53
	v_cvt_pk_bf16_f32 v221, v54, v55
	ds_write_b64 v212, v[220:221] offset:7072
	s_waitcnt lgkmcnt(8)
	s_waitcnt vmcnt(17)
	v_cvt_pk_bf16_f32 v220, v56, v57
	v_cvt_pk_bf16_f32 v221, v58, v59
	ds_write_b64 v212, v[220:221] offset:7616
	s_waitcnt lgkmcnt(8)
	s_waitcnt vmcnt(16)
	v_cvt_pk_bf16_f32 v220, v60, v61
	v_cvt_pk_bf16_f32 v221, v62, v63
	ds_write_b64 v212, v[220:221] offset:8160
	s_waitcnt lgkmcnt(0)
	ds_read_b64_tr_b16 v[222:223], v213 offset:0
	ds_read_b64_tr_b16 v[224:225], v213 offset:544
	ds_read_b64_tr_b16 v[226:227], v213 offset:4352
	ds_read_b64_tr_b16 v[228:229], v213 offset:4896
	ds_read_b64_tr_b16 v[230:231], v213 offset:32
	ds_read_b64_tr_b16 v[232:233], v213 offset:576
	ds_read_b64_tr_b16 v[234:235], v213 offset:4384
	ds_read_b64_tr_b16 v[236:237], v213 offset:4928
	s_waitcnt lgkmcnt(6)
	v_lshlrev_b32_e32 v238, 16, v222
	v_and_b32_e32 v239, 0xffff0000, v222
	v_lshlrev_b32_e32 v240, 16, v223
	v_and_b32_e32 v241, 0xffff0000, v223
	v_mul_f32_e32 v238, s11, v238
	v_mul_f32_e32 v239, s11, v239
	v_mul_f32_e32 v240, s11, v240
	v_mul_f32_e32 v241, s11, v241
	v_med3_f32 v238, v238, s12, v215
	v_med3_f32 v239, v239, s12, v215
	v_med3_f32 v240, v240, s12, v215
	v_med3_f32 v241, v241, s12, v215
	v_add_f32_e32 v238, v216, v238
	v_add_f32_e32 v239, v216, v239
	v_add_f32_e32 v240, v216, v240
	v_add_f32_e32 v241, v216, v241
	v_perm_b32 v238, v239, v238, s24
	v_perm_b32 v240, v241, v240, s24
	v_lshl_or_b32 v246, v240, 16, v238
	v_lshlrev_b32_e32 v238, 16, v224
	v_and_b32_e32 v239, 0xffff0000, v224
	v_lshlrev_b32_e32 v240, 16, v225
	v_and_b32_e32 v241, 0xffff0000, v225
	v_mul_f32_e32 v238, s11, v238
	v_mul_f32_e32 v239, s11, v239
	v_mul_f32_e32 v240, s11, v240
	v_mul_f32_e32 v241, s11, v241
	v_med3_f32 v238, v238, s12, v215
	v_med3_f32 v239, v239, s12, v215
	v_med3_f32 v240, v240, s12, v215
	v_med3_f32 v241, v241, s12, v215
	v_add_f32_e32 v238, v216, v238
	v_add_f32_e32 v239, v216, v239
	v_add_f32_e32 v240, v216, v240
	v_add_f32_e32 v241, v216, v241
	v_perm_b32 v238, v239, v238, s24
	v_perm_b32 v240, v241, v240, s24
	v_lshl_or_b32 v247, v240, 16, v238
	global_store_dwordx2 v214, v[246:247], s[8:9]
	s_waitcnt lgkmcnt(4)
	v_lshlrev_b32_e32 v238, 16, v226
	v_and_b32_e32 v239, 0xffff0000, v226
	v_lshlrev_b32_e32 v240, 16, v227
	v_and_b32_e32 v241, 0xffff0000, v227
	v_mul_f32_e32 v238, s11, v238
	v_mul_f32_e32 v239, s11, v239
	v_mul_f32_e32 v240, s11, v240
	v_mul_f32_e32 v241, s11, v241
	v_med3_f32 v238, v238, s12, v215
	v_med3_f32 v239, v239, s12, v215
	v_med3_f32 v240, v240, s12, v215
	v_med3_f32 v241, v241, s12, v215
	v_add_f32_e32 v238, v216, v238
	v_add_f32_e32 v239, v216, v239
	v_add_f32_e32 v240, v216, v240
	v_add_f32_e32 v241, v216, v241
	v_perm_b32 v238, v239, v238, s24
	v_perm_b32 v240, v241, v240, s24
	v_lshl_or_b32 v248, v240, 16, v238
	v_lshlrev_b32_e32 v238, 16, v228
	v_and_b32_e32 v239, 0xffff0000, v228
	v_lshlrev_b32_e32 v240, 16, v229
	v_and_b32_e32 v241, 0xffff0000, v229
	v_mul_f32_e32 v238, s11, v238
	v_mul_f32_e32 v239, s11, v239
	v_mul_f32_e32 v240, s11, v240
	v_mul_f32_e32 v241, s11, v241
	v_med3_f32 v238, v238, s12, v215
	v_med3_f32 v239, v239, s12, v215
	v_med3_f32 v240, v240, s12, v215
	v_med3_f32 v241, v241, s12, v215
	v_add_f32_e32 v238, v216, v238
	v_add_f32_e32 v239, v216, v239
	v_add_f32_e32 v240, v216, v240
	v_add_f32_e32 v241, v216, v241
	v_perm_b32 v238, v239, v238, s24
	v_perm_b32 v240, v241, v240, s24
	v_lshl_or_b32 v249, v240, 16, v238
	global_store_dwordx2 v214, v[248:249], s[8:9] offset:32
	ds_read_b64_tr_b16 v[222:223], v213 offset:64
	ds_read_b64_tr_b16 v[224:225], v213 offset:608
	ds_read_b64_tr_b16 v[226:227], v213 offset:4416
	ds_read_b64_tr_b16 v[228:229], v213 offset:4960
	s_add_u32 s8, s8, 0x4000
	s_addc_u32 s9, s9, 0
	s_waitcnt lgkmcnt(6)
; #define LAS __attribute__((address_space(3)))
; __device__ __forceinline__ unsigned q8x4(float a, float b, float c, float d, float s) { return q8_(a, s) | (q8_(b, s) << 8) | (q8_(c, s) << 16) | (q8_(d, s) << 24); }
;     ...
;     const int i16 = lane & 15, q = i16 >> 2, p = i16 & 3;
; #pragma unroll
;     for (int s = 0; s < 8; ++s) { const int nbk = s & 3, kbk = 4 * (s >> 2) + g;
;         const v4i16_t lo = __builtin_amdgcn_ds_read_tr16_b64_v4i16((LAS v4i16_t*)(scr + (8 * kbk + q) * 136 + 32 * nbk + 8 * p));
;         const v4i16_t hi = __builtin_amdgcn_ds_read_tr16_b64_v4i16((LAS v4i16_t*)(scr + (8 * kbk + 4 + q) * 136 + 32 * nbk + 8 * p));
;         const bf16x8 o = __builtin_shufflevector(lo, hi, 0, 1, 2, 3, 4, 5, 6, 7); const int n = 16 * nbk + i16;
;         if (n0 + n < nc) {
;             if constexpr (QMODE == 0) *(bf16x8*)(WT + (size_t)(r0 + n0 + n) * K + k0 + 8 * kbk) = o;
;             else { const v4u ou = __builtin_bit_cast(v4u, o); const float sc_ = QMODE == 1 ? QS_WUP : (QMODE == 2 ? QS_WDN : QS_WIN);
;                 *(v2u*)((unsigned char*)WT + (size_t)(r0 + n0 + n) * K + k0 + 8 * kbk) = (v2u){q8x4(bflo(ou.x), bfhi(ou.x), bflo(ou.y), bfhi(ou.y), sc_), q8x4(bflo(ou.z), bfhi(ou.z), bflo(ou.w), bfhi(ou.w), sc_)}; } } }
	v_lshlrev_b32_e32 v238, 16, v230
	v_and_b32_e32 v239, 0xffff0000, v230
	v_lshlrev_b32_e32 v240, 16, v231
	v_and_b32_e32 v241, 0xffff0000, v231
	v_mul_f32_e32 v238, s11, v238
	v_mul_f32_e32 v239, s11, v239
	v_mul_f32_e32 v240, s11, v240
	v_mul_f32_e32 v241, s11, v241
	v_med3_f32 v238, v238, s12, v215
	v_med3_f32 v239, v239, s12, v215
	v_med3_f32 v240, v240, s12, v215
	v_med3_f32 v241, v241, s12, v215
	v_add_f32_e32 v238, v216, v238
	v_add_f32_e32 v239, v216, v239
	v_add_f32_e32 v240, v216, v240
	v_add_f32_e32 v241, v216, v241
	v_perm_b32 v238, v239, v238, s24
	v_perm_b32 v240, v241, v240, s24
	v_lshl_or_b32 v246, v240, 16, v238
	v_lshlrev_b32_e32 v238, 16, v232
	v_and_b32_e32 v239, 0xffff0000, v232
	v_lshlrev_b32_e32 v240, 16, v233
	v_and_b32_e32 v241, 0xffff0000, v233
	v_mul_f32_e32 v238, s11, v238
	v_mul_f32_e32 v239, s11, v239
	v_mul_f32_e32 v240, s11, v240
	v_mul_f32_e32 v241, s11, v241
	v_med3_f32 v238, v238, s12, v215
	v_med3_f32 v239, v239, s12, v215
	v_med3_f32 v240, v240, s12, v215
	v_med3_f32 v241, v241, s12, v215
	v_add_f32_e32 v238, v216, v238
	v_add_f32_e32 v239, v216, v239
	v_add_f32_e32 v240, v216, v240
	v_add_f32_e32 v241, v216, v241
	v_perm_b32 v238, v239, v238, s24
	v_perm_b32 v240, v241, v240, s24
	v_lshl_or_b32 v247, v240, 16, v238
	global_store_dwordx2 v214, v[246:247], s[8:9]
	s_waitcnt lgkmcnt(4)
	v_lshlrev_b32_e32 v238, 16, v234
	v_and_b32_e32 v239, 0xffff0000, v234
	v_lshlrev_b32_e32 v240, 16, v235
	v_and_b32_e32 v241, 0xffff0000, v235
	v_mul_f32_e32 v238, s11, v238
	v_mul_f32_e32 v239, s11, v239
	v_mul_f32_e32 v240, s11, v240
	v_mul_f32_e32 v241, s11, v241
	v_med3_f32 v238, v238, s12, v215
	v_med3_f32 v239, v239, s12, v215
	v_med3_f32 v240, v240, s12, v215
	v_med3_f32 v241, v241, s12, v215
	v_add_f32_e32 v238, v216, v238
	v_add_f32_e32 v239, v216, v239
	v_add_f32_e32 v240, v216, v240
	v_add_f32_e32 v241, v216, v241
	v_perm_b32 v238, v239, v238, s24
	v_perm_b32 v240, v241, v240, s24
	v_lshl_or_b32 v248, v240, 16, v238
	v_lshlrev_b32_e32 v238, 16, v236
	v_and_b32_e32 v239, 0xffff0000, v236
	v_lshlrev_b32_e32 v240, 16, v237
	v_and_b32_e32 v241, 0xffff0000, v237
	v_mul_f32_e32 v238, s11, v238
	v_mul_f32_e32 v239, s11, v239
	v_mul_f32_e32 v240, s11, v240
	v_mul_f32_e32 v241, s11, v241
	v_med3_f32 v238, v238, s12, v215
	v_med3_f32 v239, v239, s12, v215
	v_med3_f32 v240, v240, s12, v215
	v_med3_f32 v241, v241, s12, v215
	v_add_f32_e32 v238, v216, v238
	v_add_f32_e32 v239, v216, v239
	v_add_f32_e32 v240, v216, v240
	v_add_f32_e32 v241, v216, v241
	v_perm_b32 v238, v239, v238, s24
	v_perm_b32 v240, v241, v240, s24
	v_lshl_or_b32 v249, v240, 16, v238
	global_store_dwordx2 v214, v[248:249], s[8:9] offset:32
	ds_read_b64_tr_b16 v[230:231], v213 offset:96
	ds_read_b64_tr_b16 v[232:233], v213 offset:640
	ds_read_b64_tr_b16 v[234:235], v213 offset:4448
	ds_read_b64_tr_b16 v[236:237], v213 offset:4992
	s_add_u32 s8, s8, 0x4000
	s_addc_u32 s9, s9, 0
	s_waitcnt lgkmcnt(6)
	v_lshlrev_b32_e32 v238, 16, v222
	v_and_b32_e32 v239, 0xffff0000, v222
	v_lshlrev_b32_e32 v240, 16, v223
	v_and_b32_e32 v241, 0xffff0000, v223
	v_mul_f32_e32 v238, s11, v238
	v_mul_f32_e32 v239, s11, v239
	v_mul_f32_e32 v240, s11, v240
	v_mul_f32_e32 v241, s11, v241
	v_med3_f32 v238, v238, s12, v215
	v_med3_f32 v239, v239, s12, v215
	v_med3_f32 v240, v240, s12, v215
	v_med3_f32 v241, v241, s12, v215
	v_add_f32_e32 v238, v216, v238
	v_add_f32_e32 v239, v216, v239
	v_add_f32_e32 v240, v216, v240
	v_add_f32_e32 v241, v216, v241
	v_perm_b32 v238, v239, v238, s24
	v_perm_b32 v240, v241, v240, s24
	v_lshl_or_b32 v246, v240, 16, v238
	v_lshlrev_b32_e32 v238, 16, v224
	v_and_b32_e32 v239, 0xffff0000, v224
	v_lshlrev_b32_e32 v240, 16, v225
	v_and_b32_e32 v241, 0xffff0000, v225
	v_mul_f32_e32 v238, s11, v238
	v_mul_f32_e32 v239, s11, v239
	v_mul_f32_e32 v240, s11, v240
	v_mul_f32_e32 v241, s11, v241
	v_med3_f32 v238, v238, s12, v215
	v_med3_f32 v239, v239, s12, v215
	v_med3_f32 v240, v240, s12, v215
	v_med3_f32 v241, v241, s12, v215
	v_add_f32_e32 v238, v216, v238
	v_add_f32_e32 v239, v216, v239
	v_add_f32_e32 v240, v216, v240
	v_add_f32_e32 v241, v216, v241
	v_perm_b32 v238, v239, v238, s24
	v_perm_b32 v240, v241, v240, s24
	v_lshl_or_b32 v247, v240, 16, v238
	global_store_dwordx2 v214, v[246:247], s[8:9]
	s_waitcnt lgkmcnt(4)
; #define LAS __attribute__((address_space(3)))
; __device__ __forceinline__ unsigned q8x4(float a, float b, float c, float d, float s) { return q8_(a, s) | (q8_(b, s) << 8) | (q8_(c, s) << 16) | (q8_(d, s) << 24); }
;     ...
;     const int i16 = lane & 15, q = i16 >> 2, p = i16 & 3;
; #pragma unroll
;     for (int s = 0; s < 8; ++s) { const int nbk = s & 3, kbk = 4 * (s >> 2) + g;
;         const v4i16_t lo = __builtin_amdgcn_ds_read_tr16_b64_v4i16((LAS v4i16_t*)(scr + (8 * kbk + q) * 136 + 32 * nbk + 8 * p));
;         const v4i16_t hi = __builtin_amdgcn_ds_read_tr16_b64_v4i16((LAS v4i16_t*)(scr + (8 * kbk + 4 + q) * 136 + 32 * nbk + 8 * p));
;         const bf16x8 o = __builtin_shufflevector(lo, hi, 0, 1, 2, 3, 4, 5, 6, 7); const int n = 16 * nbk + i16;
;         if (n0 + n < nc) {
;             if constexpr (QMODE == 0) *(bf16x8*)(WT + (size_t)(r0 + n0 + n) * K + k0 + 8 * kbk) = o;
;             else { const v4u ou = __builtin_bit_cast(v4u, o); const float sc_ = QMODE == 1 ? QS_WUP : (QMODE == 2 ? QS_WDN : QS_WIN);
;                 *(v2u*)((unsigned char*)WT + (size_t)(r0 + n0 + n) * K + k0 + 8 * kbk) = (v2u){q8x4(bflo(ou.x), bfhi(ou.x), bflo(ou.y), bfhi(ou.y), sc_), q8x4(bflo(ou.z), bfhi(ou.z), bflo(ou.w), bfhi(ou.w), sc_)}; } } }
; __global__ void __launch_bounds__(NWAVES * 64, 2) fwd(Args args) {
;     ...
;         for (;;) { int base_ = 0; if (lane == 0) base_ = (int)__hip_atomic_fetch_add(CTLP + CW_Q0, 4u, RLX_AGENT); base_ = __builtin_amdgcn_readfirstlane(base_); if (base_ >= NL * I_LAYER) break;
;         for (int it = base_; it < base_ + 4 && it < NL * I_LAYER; ++it) {
;             const int l = it / I_LAYER; int r = it % I_LAYER;
;             const float* Wl = w_in + (size_t)l * D * DIN; bf16* Wt = (bf16*)((unsigned char*)WinT + (size_t)l * NP * D);
;             if (r < I_WIN) {
;                 if (r < I_CKV) { tr_item64<3>(Wl, DIN, SC_CKV, 128, D, Wt, PC_CKV, scr, r, lane); continue; } r -= I_CKV;
	v_lshlrev_b32_e32 v238, 16, v226
	v_and_b32_e32 v239, 0xffff0000, v226
	v_lshlrev_b32_e32 v240, 16, v227
	v_and_b32_e32 v241, 0xffff0000, v227
	v_mul_f32_e32 v238, s11, v238
	v_mul_f32_e32 v239, s11, v239
	v_mul_f32_e32 v240, s11, v240
	v_mul_f32_e32 v241, s11, v241
	v_med3_f32 v238, v238, s12, v215
	v_med3_f32 v239, v239, s12, v215
	v_med3_f32 v240, v240, s12, v215
	v_med3_f32 v241, v241, s12, v215
	v_add_f32_e32 v238, v216, v238
	v_add_f32_e32 v239, v216, v239
	v_add_f32_e32 v240, v216, v240
	v_add_f32_e32 v241, v216, v241
	v_perm_b32 v238, v239, v238, s24
	v_perm_b32 v240, v241, v240, s24
	v_lshl_or_b32 v248, v240, 16, v238
	v_lshlrev_b32_e32 v238, 16, v228
	v_and_b32_e32 v239, 0xffff0000, v228
	v_lshlrev_b32_e32 v240, 16, v229
	v_and_b32_e32 v241, 0xffff0000, v229
	v_mul_f32_e32 v238, s11, v238
	v_mul_f32_e32 v239, s11, v239
	v_mul_f32_e32 v240, s11, v240
	v_mul_f32_e32 v241, s11, v241
	v_med3_f32 v238, v238, s12, v215
	v_med3_f32 v239, v239, s12, v215
	v_med3_f32 v240, v240, s12, v215
	v_med3_f32 v241, v241, s12, v215
	v_add_f32_e32 v238, v216, v238
	v_add_f32_e32 v239, v216, v239
	v_add_f32_e32 v240, v216, v240
	v_add_f32_e32 v241, v216, v241
	v_perm_b32 v238, v239, v238, s24
	v_perm_b32 v240, v241, v240, s24
	v_lshl_or_b32 v249, v240, 16, v238
	global_store_dwordx2 v214, v[248:249], s[8:9] offset:32
	s_add_u32 s8, s8, 0x4000
	s_addc_u32 s9, s9, 0
	s_waitcnt lgkmcnt(2)
	v_lshlrev_b32_e32 v238, 16, v230
	v_and_b32_e32 v239, 0xffff0000, v230
	v_lshlrev_b32_e32 v240, 16, v231
	v_and_b32_e32 v241, 0xffff0000, v231
	v_mul_f32_e32 v238, s11, v238
	v_mul_f32_e32 v239, s11, v239
	v_mul_f32_e32 v240, s11, v240
	v_mul_f32_e32 v241, s11, v241
	v_med3_f32 v238, v238, s12, v215
	v_med3_f32 v239, v239, s12, v215
	v_med3_f32 v240, v240, s12, v215
	v_med3_f32 v241, v241, s12, v215
	v_add_f32_e32 v238, v216, v238
	v_add_f32_e32 v239, v216, v239
	v_add_f32_e32 v240, v216, v240
	v_add_f32_e32 v241, v216, v241
	v_perm_b32 v238, v239, v238, s24
	v_perm_b32 v240, v241, v240, s24
	v_lshl_or_b32 v246, v240, 16, v238
	v_lshlrev_b32_e32 v238, 16, v232
	v_and_b32_e32 v239, 0xffff0000, v232
	v_lshlrev_b32_e32 v240, 16, v233
	v_and_b32_e32 v241, 0xffff0000, v233
	v_mul_f32_e32 v238, s11, v238
	v_mul_f32_e32 v239, s11, v239
	v_mul_f32_e32 v240, s11, v240
	v_mul_f32_e32 v241, s11, v241
	v_med3_f32 v238, v238, s12, v215
	v_med3_f32 v239, v239, s12, v215
	v_med3_f32 v240, v240, s12, v215
	v_med3_f32 v241, v241, s12, v215
	v_add_f32_e32 v238, v216, v238
	v_add_f32_e32 v239, v216, v239
	v_add_f32_e32 v240, v216, v240
	v_add_f32_e32 v241, v216, v241
	v_perm_b32 v238, v239, v238, s24
	v_perm_b32 v240, v241, v240, s24
	v_lshl_or_b32 v247, v240, 16, v238
	global_store_dwordx2 v214, v[246:247], s[8:9]
	s_waitcnt lgkmcnt(0)
	v_lshlrev_b32_e32 v238, 16, v234
	v_and_b32_e32 v239, 0xffff0000, v234
	v_lshlrev_b32_e32 v240, 16, v235
	v_and_b32_e32 v241, 0xffff0000, v235
	v_mul_f32_e32 v238, s11, v238
	v_mul_f32_e32 v239, s11, v239
	v_mul_f32_e32 v240, s11, v240
	v_mul_f32_e32 v241, s11, v241
	v_med3_f32 v238, v238, s12, v215
	v_med3_f32 v239, v239, s12, v215
	v_med3_f32 v240, v240, s12, v215
	v_med3_f32 v241, v241, s12, v215
	v_add_f32_e32 v238, v216, v238
	v_add_f32_e32 v239, v216, v239
	v_add_f32_e32 v240, v216, v240
	v_add_f32_e32 v241, v216, v241
	v_perm_b32 v238, v239, v238, s24
	v_perm_b32 v240, v241, v240, s24
	v_lshl_or_b32 v248, v240, 16, v238
	v_lshlrev_b32_e32 v238, 16, v236
	v_and_b32_e32 v239, 0xffff0000, v236
	v_lshlrev_b32_e32 v240, 16, v237
	v_and_b32_e32 v241, 0xffff0000, v237
	v_mul_f32_e32 v238, s11, v238
	v_mul_f32_e32 v239, s11, v239
	v_mul_f32_e32 v240, s11, v240
	v_mul_f32_e32 v241, s11, v241
	v_med3_f32 v238, v238, s12, v215
	v_med3_f32 v239, v239, s12, v215
	v_med3_f32 v240, v240, s12, v215
	v_med3_f32 v241, v241, s12, v215
	v_add_f32_e32 v238, v216, v238
	v_add_f32_e32 v239, v216, v239
	v_add_f32_e32 v240, v216, v240
	v_add_f32_e32 v241, v216, v241
	v_perm_b32 v238, v239, v238, s24
	v_perm_b32 v240, v241, v240, s24
	v_lshl_or_b32 v249, v240, 16, v238
	global_store_dwordx2 v214, v[248:249], s[8:9] offset:32
	s_sub_u32 s8, s8, 0xbfc0
	s_subb_u32 s9, s9, 0
	s_branch .LBB0_63
.Lp0f_slow:
	s_lshl_b32 s6, s96, 4
	s_add_i32 s37, s6, 0xe00
	s_lshl_b32 s6, s96, 2
	s_lshl_b32 s26, s96, 6
	s_lshl_b32 s38, s96, 3
	s_add_i32 s39, s6, 0x7ffffe00
	s_branch .LBB0_74
